# combine-L0 to W-L1 grid barrier removed (no dependency); LRU epilogue x rows requested up front
# baseline (speedup 1.0000x reference)
.LBB0_521:
	s_lshl_b32 s39, s46, 6
	s_lshl_b32 s45, s46, 7
	s_and_b32 s39, s39, 0xffffff00
	s_and_b32 s45, s45, 0x80
	s_bfe_u32 s37, s46, 0x10001
	s_or_b32 s39, s39, s45
	v_add_u32_e32 v160, s39, v164
	s_lshl_b32 s39, s37, 12
	s_add_u32 s46, s6, s39
	v_ashrrev_i32_e32 v161, 31, v160
	s_addc_u32 s47, s7, 0
	v_lshlrev_b64 v[140:141], 2, v[160:161]
	v_lshl_add_u64 v[146:147], s[46:47], 0, v[140:141]
	global_load_dwordx4 v[142:145], v[146:147], off offset:16
	s_nop 0
	global_load_dwordx4 v[146:149], v[146:147], off
	v_lshl_add_u32 v152, s44, 8, v163
	v_ashrrev_i32_e32 v153, 31, v152
	v_lshlrev_b64 v[150:151], 11, v[152:153]
	v_lshl_add_u64 v[150:151], s[10:11], 0, v[150:151]
	v_lshlrev_b64 v[154:155], 1, v[160:161]
	s_add_u32 s44, s8, s39
	v_lshl_add_u64 v[150:151], v[150:151], 0, v[154:155]
	s_addc_u32 s45, s9, 0
	global_load_dwordx4 v[168:171], v[150:151], off
	s_mov_b32 s99, 0
	s_mov_b32 s98, 0x8000
	v_lshl_add_u64 v[224:225], v[150:151], 0, s[98:99]
	global_load_dwordx4 v[196:199], v[224:225], off
	s_mov_b32 s98, 0x10000
	v_lshl_add_u64 v[228:229], v[150:151], 0, s[98:99]
	global_load_dwordx4 v[200:203], v[228:229], off
	s_mov_b32 s98, 0x18000
	v_lshl_add_u64 v[224:225], v[150:151], 0, s[98:99]
	global_load_dwordx4 v[204:207], v[224:225], off
	s_mov_b32 s98, 0x40000
	v_lshl_add_u64 v[228:229], v[150:151], 0, s[98:99]
	global_load_dwordx4 v[208:211], v[228:229], off
	s_mov_b32 s98, 0x48000
	v_lshl_add_u64 v[224:225], v[150:151], 0, s[98:99]
	global_load_dwordx4 v[212:215], v[224:225], off
	s_mov_b32 s98, 0x50000
	v_lshl_add_u64 v[228:229], v[150:151], 0, s[98:99]
	global_load_dwordx4 v[216:219], v[228:229], off
	s_mov_b32 s98, 0x58000
	v_lshl_add_u64 v[224:225], v[150:151], 0, s[98:99]
	global_load_dwordx4 v[220:223], v[224:225], off
	v_lshl_add_u64 v[150:151], s[44:45], 0, v[140:141]
	global_load_dwordx4 v[172:175], v[150:151], off
	global_load_dwordx4 v[176:179], v[150:151], off offset:16
	s_add_u32 s44, s62, s39
	s_addc_u32 s45, s63, 0
	v_lshl_add_u64 v[140:141], s[44:45], 0, v[140:141]
	global_load_dwordx4 v[180:183], v[140:141], off
	global_load_dwordx4 v[184:187], v[140:141], off offset:16
	s_mul_i32 s37, s37, 0x4400000
	s_add_u32 s44, s58, s37
	s_addc_u32 s45, s59, 0
	s_add_u32 s46, s60, s37
	s_addc_u32 s47, s61, 0
	s_andn2_b64 vcc, exec, s[2:3]
	s_mov_b64 s[2:3], -1
	s_waitcnt vmcnt(0)
	v_pk_mul_f32 v[142:143], v[142:143], s[24:25] op_sel_hi:[1,0]
	v_pk_mul_f32 v[148:149], v[148:149], s[24:25] op_sel_hi:[1,0]
	v_pk_mul_f32 v[150:151], v[146:147], s[24:25] op_sel_hi:[1,0]
	v_fmamk_f32 v126, v126, 0xbfb8aa3b, v148
	v_fmamk_f32 v124, v124, 0xbfb8aa3b, v150
	v_fmamk_f32 v125, v125, 0xbfb8aa3b, v151
	v_fmamk_f32 v127, v127, 0xbfb8aa3b, v149
	v_exp_f32_e32 v124, v124
	v_exp_f32_e32 v125, v125
	v_exp_f32_e32 v126, v126
	v_exp_f32_e32 v127, v127
	v_pk_mul_f32 v[158:159], v[172:173], s[24:25] op_sel_hi:[1,0]
	v_pk_mul_f32 v[156:157], v[174:175], s[24:25] op_sel_hi:[1,0]
	v_pk_mul_f32 v[146:147], v[176:177], s[24:25] op_sel_hi:[1,0]
	v_fmamk_f32 v174, v120, 0xbfb8aa3b, v158
	v_fmamk_f32 v176, v121, 0xbfb8aa3b, v159
	v_pk_add_f32 v[126:127], v[126:127], 1.0 op_sel_hi:[1,0]
	v_pk_add_f32 v[124:125], v[124:125], 1.0 op_sel_hi:[1,0]
	v_fmamk_f32 v190, v116, 0xbfb8aa3b, v146
	v_fmamk_f32 v191, v117, 0xbfb8aa3b, v147
	v_exp_f32_e32 v116, v174
	v_exp_f32_e32 v117, v176
	v_rcp_f32_e32 v124, v124
	v_rcp_f32_e32 v125, v125
	v_rcp_f32_e32 v126, v126
	v_rcp_f32_e32 v127, v127
	v_fmamk_f32 v175, v122, 0xbfb8aa3b, v156
	v_fmamk_f32 v177, v123, 0xbfb8aa3b, v157
	v_pk_mul_f32 v[122:123], v[182:183], s[26:27] op_sel_hi:[1,0]
	v_pk_mul_f32 v[120:121], v[180:181], s[26:27] op_sel_hi:[1,0]
	v_pk_add_f32 v[116:117], v[116:117], 1.0 op_sel_hi:[1,0]
	v_pk_mul_f32 v[126:127], v[122:123], v[126:127]
	v_pk_mul_f32 v[124:125], v[120:121], v[124:125]
	v_pk_mul_f32 v[140:141], v[144:145], s[24:25] op_sel_hi:[1,0]
	v_pk_mul_f32 v[144:145], v[178:179], s[24:25] op_sel_hi:[1,0]
	v_fmamk_f32 v112, v112, 0xbfb8aa3b, v142
	v_fmamk_f32 v113, v113, 0xbfb8aa3b, v143
	v_exp_f32_e32 v174, v175
	v_exp_f32_e32 v175, v177
	v_rcp_f32_e32 v176, v116
	v_rcp_f32_e32 v177, v117
	v_mul_f32_e32 v116, 0x4038aa3b, v124
	v_mul_f32_e32 v117, 0x4038aa3b, v125
	v_mul_f32_e32 v178, 0x4038aa3b, v127
	v_fmamk_f32 v114, v114, 0xbfb8aa3b, v140
	v_exp_f32_e32 v172, v112
	v_exp_f32_e32 v173, v113
	v_fmamk_f32 v192, v118, 0xbfb8aa3b, v144
	v_mul_f32_e32 v118, 0x4038aa3b, v126
	v_exp_f32_e32 v178, v178
	v_exp_f32_e32 v117, v117
	v_exp_f32_e32 v116, v116
	v_fmamk_f32 v115, v115, 0xbfb8aa3b, v141
	v_exp_f32_e32 v114, v114
	v_exp_f32_e32 v118, v118
	v_exp_f32_e32 v115, v115
	v_sub_f32_e32 v178, 1.0, v178
	v_sub_f32_e32 v117, 1.0, v117
	v_sub_f32_e32 v116, 1.0, v116
	v_pk_add_f32 v[172:173], v[172:173], 1.0 op_sel_hi:[1,0]
	v_sub_f32_e32 v118, 1.0, v118
	v_max_f32_e32 v116, 0, v116
	v_max_f32_e32 v117, 0, v117
	v_max_f32_e32 v179, 0, v178
	v_pk_add_f32 v[114:115], v[114:115], 1.0 op_sel_hi:[1,0]
	v_rcp_f32_e32 v172, v172
	v_rcp_f32_e32 v173, v173
	v_pk_add_f32 v[174:175], v[174:175], 1.0 op_sel_hi:[1,0]
	v_max_f32_e32 v118, 0, v118
	v_sqrt_f32_e32 v178, v116
	v_sqrt_f32_e32 v181, v179
	v_sqrt_f32_e32 v179, v117
	v_rcp_f32_e32 v114, v114
	v_rcp_f32_e32 v115, v115
	v_rcp_f32_e32 v174, v174
	v_rcp_f32_e32 v175, v175
	v_sqrt_f32_e32 v180, v118
	v_pk_mul_f32 v[116:117], v[184:185], s[26:27] op_sel_hi:[1,0]
	v_pk_mul_f32 v[112:113], v[186:187], s[26:27] op_sel_hi:[1,0]
	v_pk_mul_f32 v[172:173], v[116:117], v[172:173]
	v_pk_mul_f32 v[176:177], v[176:177], v[178:179]
	v_pk_mul_f32 v[114:115], v[112:113], v[114:115]
	v_mul_f32_e32 v178, 0x4038aa3b, v172
	v_mul_f32_e32 v179, 0x4038aa3b, v173
	v_lshlrev_b32_e32 v188, 16, v168
	v_and_b32_e32 v189, 0xffff0000, v168
	v_lshlrev_b32_e32 v168, 16, v169
	v_and_b32_e32 v169, 0xffff0000, v169
	v_pk_mul_f32 v[174:175], v[174:175], v[180:181]
	v_fmamk_f32 v119, v119, 0xbfb8aa3b, v145
	v_mul_f32_e32 v180, 0x4038aa3b, v114
	v_mul_f32_e32 v181, 0x4038aa3b, v115
	v_exp_f32_e32 v179, v179
	v_exp_f32_e32 v178, v178
	v_exp_f32_e32 v118, v190
	v_pk_mul_f32 v[174:175], v[174:175], v[168:169]
	v_pk_mul_f32 v[168:169], v[176:177], v[188:189]
	v_exp_f32_e32 v177, v119
	v_exp_f32_e32 v119, v191
	v_exp_f32_e32 v181, v181
	v_exp_f32_e32 v180, v180
	v_exp_f32_e32 v176, v192
	v_sub_f32_e32 v179, 1.0, v179
	v_sub_f32_e32 v178, 1.0, v178
	v_pk_add_f32 v[118:119], v[118:119], 1.0 op_sel_hi:[1,0]
	v_sub_f32_e32 v181, 1.0, v181
	v_sub_f32_e32 v180, 1.0, v180
	v_max_f32_e32 v178, 0, v178
	v_max_f32_e32 v179, 0, v179
	v_pk_add_f32 v[176:177], v[176:177], 1.0 op_sel_hi:[1,0]
	v_rcp_f32_e32 v118, v118
	v_rcp_f32_e32 v119, v119
	v_sqrt_f32_e32 v178, v178
	v_sqrt_f32_e32 v179, v179
	v_max_f32_e32 v180, 0, v180
	v_max_f32_e32 v181, 0, v181
	v_rcp_f32_e32 v176, v176
	v_rcp_f32_e32 v177, v177
	v_sqrt_f32_e32 v180, v180
	v_sqrt_f32_e32 v181, v181
	v_lshlrev_b32_e32 v182, 16, v170
	v_and_b32_e32 v183, 0xffff0000, v170
	v_pk_mul_f32 v[118:119], v[118:119], v[178:179]
	v_lshlrev_b32_e32 v170, 16, v171
	v_and_b32_e32 v171, 0xffff0000, v171
	v_pk_mul_f32 v[176:177], v[176:177], v[180:181]
	v_pk_mul_f32 v[118:119], v[118:119], v[182:183]
	v_pk_mul_f32 v[176:177], v[176:177], v[170:171]
	v_cvt_pk_bf16_f32 v124, v124, v125
	v_cvt_pk_bf16_f32 v125, v126, v127
	v_cvt_pk_bf16_f32 v126, v172, v173
	v_cvt_pk_bf16_f32 v127, v114, v115
	v_cvt_pk_bf16_f32 v168, v168, v169
	v_cvt_pk_bf16_f32 v169, v174, v175
	v_cvt_pk_bf16_f32 v170, v118, v119
	v_or_b32_e32 v118, 16, v152
	v_ashrrev_i32_e32 v119, 31, v118
	v_lshlrev_b64 v[114:115], 11, v[118:119]
	v_lshl_add_u64 v[114:115], s[10:11], 0, v[114:115]
	v_cvt_pk_bf16_f32 v171, v176, v177
	v_lshl_add_u64 v[114:115], v[114:115], 0, v[154:155]
	v_mov_b64_e32 v[172:173], v[196:197]
	v_mov_b64_e32 v[174:175], v[198:199]
	v_fmamk_f32 v104, v104, 0xbfb8aa3b, v150
	v_fmamk_f32 v105, v105, 0xbfb8aa3b, v151
	v_exp_f32_e32 v104, v104
	v_exp_f32_e32 v105, v105
	v_fmamk_f32 v106, v106, 0xbfb8aa3b, v148
	v_fmamk_f32 v107, v107, 0xbfb8aa3b, v149
	v_exp_f32_e32 v106, v106
	v_exp_f32_e32 v107, v107
	v_pk_add_f32 v[104:105], v[104:105], 1.0 op_sel_hi:[1,0]
	v_lshlrev_b64 v[114:115], 10, v[152:153]
	v_rcp_f32_e32 v104, v104
	v_pk_add_f32 v[106:107], v[106:107], 1.0 op_sel_hi:[1,0]
	v_rcp_f32_e32 v105, v105
	v_lshl_add_u64 v[114:115], v[114:115], 0, v[160:161]
	v_rcp_f32_e32 v106, v106
	v_rcp_f32_e32 v107, v107
	v_lshlrev_b64 v[114:115], 1, v[114:115]
	v_lshl_add_u64 v[176:177], s[44:45], 0, v[114:115]
	global_store_dwordx4 v[176:177], v[124:127], off
	v_pk_mul_f32 v[104:105], v[120:121], v[104:105]
	v_pk_mul_f32 v[106:107], v[122:123], v[106:107]
	v_lshl_add_u64 v[124:125], s[46:47], 0, v[114:115]
	global_store_dwordx4 v[124:125], v[168:171], off
	v_mul_f32_e32 v124, 0x4038aa3b, v104
	v_mul_f32_e32 v125, 0x4038aa3b, v105
	v_fmamk_f32 v108, v108, 0xbfb8aa3b, v158
	v_fmamk_f32 v109, v109, 0xbfb8aa3b, v159
	v_mul_f32_e32 v126, 0x4038aa3b, v106
	v_mul_f32_e32 v127, 0x4038aa3b, v107
	v_exp_f32_e32 v125, v125
	v_exp_f32_e32 v124, v124
	v_fmamk_f32 v96, v96, 0xbfb8aa3b, v142
	v_fmamk_f32 v97, v97, 0xbfb8aa3b, v143
	v_fmamk_f32 v98, v98, 0xbfb8aa3b, v140
	v_fmamk_f32 v99, v99, 0xbfb8aa3b, v141
	v_exp_f32_e32 v108, v108
	v_fmamk_f32 v110, v110, 0xbfb8aa3b, v156
	v_fmamk_f32 v111, v111, 0xbfb8aa3b, v157
	v_exp_f32_e32 v109, v109
	v_exp_f32_e32 v127, v127
	v_exp_f32_e32 v126, v126
	v_exp_f32_e32 v96, v96
	v_exp_f32_e32 v97, v97
	v_exp_f32_e32 v98, v98
	v_exp_f32_e32 v99, v99
	v_exp_f32_e32 v110, v110
	v_exp_f32_e32 v111, v111
	v_sub_f32_e32 v125, 1.0, v125
	v_sub_f32_e32 v124, 1.0, v124
	v_pk_add_f32 v[108:109], v[108:109], 1.0 op_sel_hi:[1,0]
	v_sub_f32_e32 v127, 1.0, v127
	v_sub_f32_e32 v126, 1.0, v126
	v_max_f32_e32 v124, 0, v124
	v_max_f32_e32 v125, 0, v125
	v_pk_add_f32 v[98:99], v[98:99], 1.0 op_sel_hi:[1,0]
	v_pk_add_f32 v[96:97], v[96:97], 1.0 op_sel_hi:[1,0]
	v_pk_add_f32 v[110:111], v[110:111], 1.0 op_sel_hi:[1,0]
	v_rcp_f32_e32 v108, v108
	v_rcp_f32_e32 v109, v109
	v_sqrt_f32_e32 v124, v124
	v_sqrt_f32_e32 v125, v125
	v_max_f32_e32 v126, 0, v126
	v_max_f32_e32 v127, 0, v127
	v_rcp_f32_e32 v96, v96
	v_rcp_f32_e32 v97, v97
	v_rcp_f32_e32 v98, v98
	v_rcp_f32_e32 v99, v99
	v_rcp_f32_e32 v110, v110
	v_rcp_f32_e32 v111, v111
	v_sqrt_f32_e32 v126, v126
	v_sqrt_f32_e32 v127, v127
	v_pk_mul_f32 v[108:109], v[108:109], v[124:125]
	v_pk_mul_f32 v[124:125], v[112:113], v[98:99]
	v_pk_mul_f32 v[98:99], v[116:117], v[96:97]
	v_pk_mul_f32 v[110:111], v[110:111], v[126:127]
	v_mul_f32_e32 v96, 0x4038aa3b, v98
	v_mul_f32_e32 v97, 0x4038aa3b, v99
	v_mul_f32_e32 v126, 0x4038aa3b, v124
	v_mul_f32_e32 v127, 0x4038aa3b, v125
	v_fmamk_f32 v100, v100, 0xbfb8aa3b, v146
	v_fmamk_f32 v101, v101, 0xbfb8aa3b, v147
	v_fmamk_f32 v102, v102, 0xbfb8aa3b, v144
	v_fmamk_f32 v103, v103, 0xbfb8aa3b, v145
	v_exp_f32_e32 v127, v127
	v_exp_f32_e32 v126, v126
	v_exp_f32_e32 v97, v97
	v_exp_f32_e32 v96, v96
	v_exp_f32_e32 v100, v100
	v_exp_f32_e32 v102, v102
	v_exp_f32_e32 v103, v103
	v_exp_f32_e32 v101, v101
	v_sub_f32_e32 v127, 1.0, v127
	v_sub_f32_e32 v126, 1.0, v126
	v_sub_f32_e32 v97, 1.0, v97
	v_sub_f32_e32 v96, 1.0, v96
	v_pk_add_f32 v[102:103], v[102:103], 1.0 op_sel_hi:[1,0]
	v_pk_add_f32 v[100:101], v[100:101], 1.0 op_sel_hi:[1,0]
	v_max_f32_e32 v96, 0, v96
	v_max_f32_e32 v97, 0, v97
	v_max_f32_e32 v126, 0, v126
	v_max_f32_e32 v127, 0, v127
	v_rcp_f32_e32 v100, v100
	v_rcp_f32_e32 v101, v101
	v_rcp_f32_e32 v102, v102
	v_rcp_f32_e32 v103, v103
	v_sqrt_f32_e32 v96, v96
	v_sqrt_f32_e32 v97, v97
	v_sqrt_f32_e32 v126, v126
	v_sqrt_f32_e32 v127, v127
	s_waitcnt vmcnt(2)
	v_lshlrev_b32_e32 v168, 16, v172
	v_and_b32_e32 v169, 0xffff0000, v172
	v_lshlrev_b32_e32 v170, 16, v173
	v_and_b32_e32 v171, 0xffff0000, v173
	v_pk_mul_f32 v[110:111], v[110:111], v[170:171]
	v_pk_mul_f32 v[108:109], v[108:109], v[168:169]
	v_lshlrev_b32_e32 v168, 16, v174
	v_and_b32_e32 v169, 0xffff0000, v174
	v_lshlrev_b32_e32 v170, 16, v175
	v_and_b32_e32 v171, 0xffff0000, v175
	v_pk_mul_f32 v[102:103], v[102:103], v[126:127]
	v_pk_mul_f32 v[96:97], v[100:101], v[96:97]
	v_pk_mul_f32 v[126:127], v[102:103], v[170:171]
	v_pk_mul_f32 v[102:103], v[96:97], v[168:169]
	v_cvt_pk_bf16_f32 v96, v104, v105
	v_cvt_pk_bf16_f32 v97, v106, v107
	v_cvt_pk_bf16_f32 v98, v98, v99
	v_cvt_pk_bf16_f32 v99, v124, v125
	v_cvt_pk_bf16_f32 v100, v108, v109
	v_or_b32_e32 v108, 32, v152
	v_ashrrev_i32_e32 v109, 31, v108
	v_lshlrev_b64 v[104:105], 11, v[108:109]
	v_lshl_add_u64 v[104:105], s[10:11], 0, v[104:105]
	v_cvt_pk_bf16_f32 v101, v110, v111
	v_cvt_pk_bf16_f32 v102, v102, v103
	v_cvt_pk_bf16_f32 v103, v126, v127
	v_lshl_add_u64 v[104:105], v[104:105], 0, v[154:155]
	v_mov_b64_e32 v[104:105], v[200:201]
	v_mov_b64_e32 v[106:107], v[202:203]
	v_fmamk_f32 v88, v88, 0xbfb8aa3b, v150
	v_fmamk_f32 v89, v89, 0xbfb8aa3b, v151
	v_exp_f32_e32 v88, v88
	v_exp_f32_e32 v89, v89
	v_fmamk_f32 v90, v90, 0xbfb8aa3b, v148
	v_fmamk_f32 v91, v91, 0xbfb8aa3b, v149
	v_exp_f32_e32 v90, v90
	v_exp_f32_e32 v91, v91
	v_pk_add_f32 v[88:89], v[88:89], 1.0 op_sel_hi:[1,0]
	v_lshlrev_b64 v[110:111], 10, v[118:119]
	v_rcp_f32_e32 v88, v88
	v_pk_add_f32 v[90:91], v[90:91], 1.0 op_sel_hi:[1,0]
	v_rcp_f32_e32 v89, v89
	v_lshl_add_u64 v[110:111], v[110:111], 0, v[160:161]
	v_rcp_f32_e32 v90, v90
	v_rcp_f32_e32 v91, v91
	v_lshlrev_b64 v[110:111], 1, v[110:111]
	v_lshl_add_u64 v[118:119], s[44:45], 0, v[110:111]
	global_store_dwordx4 v[118:119], v[96:99], off
	v_pk_mul_f32 v[88:89], v[120:121], v[88:89]
	v_pk_mul_f32 v[90:91], v[122:123], v[90:91]
	v_lshl_add_u64 v[96:97], s[46:47], 0, v[110:111]
	global_store_dwordx4 v[96:97], v[100:103], off
	v_mul_f32_e32 v96, 0x4038aa3b, v88
	v_mul_f32_e32 v97, 0x4038aa3b, v89
	v_fmamk_f32 v92, v92, 0xbfb8aa3b, v158
	v_fmamk_f32 v93, v93, 0xbfb8aa3b, v159
	v_mul_f32_e32 v98, 0x4038aa3b, v90
	v_mul_f32_e32 v99, 0x4038aa3b, v91
	v_exp_f32_e32 v97, v97
	v_exp_f32_e32 v96, v96
	v_fmamk_f32 v80, v80, 0xbfb8aa3b, v142
	v_fmamk_f32 v81, v81, 0xbfb8aa3b, v143
	v_fmamk_f32 v82, v82, 0xbfb8aa3b, v140
	v_fmamk_f32 v83, v83, 0xbfb8aa3b, v141
	v_exp_f32_e32 v92, v92
	v_fmamk_f32 v94, v94, 0xbfb8aa3b, v156
	v_fmamk_f32 v95, v95, 0xbfb8aa3b, v157
	v_exp_f32_e32 v93, v93
	v_exp_f32_e32 v99, v99
	v_exp_f32_e32 v98, v98
	v_exp_f32_e32 v80, v80
	v_exp_f32_e32 v81, v81
	v_exp_f32_e32 v82, v82
	v_exp_f32_e32 v83, v83
	v_exp_f32_e32 v94, v94
	v_exp_f32_e32 v95, v95
	v_sub_f32_e32 v97, 1.0, v97
	v_sub_f32_e32 v96, 1.0, v96
	v_pk_add_f32 v[92:93], v[92:93], 1.0 op_sel_hi:[1,0]
	v_sub_f32_e32 v99, 1.0, v99
	v_sub_f32_e32 v98, 1.0, v98
	v_max_f32_e32 v96, 0, v96
	v_max_f32_e32 v97, 0, v97
	v_pk_add_f32 v[82:83], v[82:83], 1.0 op_sel_hi:[1,0]
	v_pk_add_f32 v[80:81], v[80:81], 1.0 op_sel_hi:[1,0]
	v_pk_add_f32 v[94:95], v[94:95], 1.0 op_sel_hi:[1,0]
	v_rcp_f32_e32 v92, v92
	v_rcp_f32_e32 v93, v93
	v_sqrt_f32_e32 v96, v96
	v_sqrt_f32_e32 v97, v97
	v_max_f32_e32 v98, 0, v98
	v_max_f32_e32 v99, 0, v99
	v_rcp_f32_e32 v80, v80
	v_rcp_f32_e32 v81, v81
	v_rcp_f32_e32 v82, v82
	v_rcp_f32_e32 v83, v83
	v_rcp_f32_e32 v94, v94
	v_rcp_f32_e32 v95, v95
	v_sqrt_f32_e32 v98, v98
	v_sqrt_f32_e32 v99, v99
	v_pk_mul_f32 v[92:93], v[92:93], v[96:97]
	v_pk_mul_f32 v[96:97], v[112:113], v[82:83]
	v_pk_mul_f32 v[82:83], v[116:117], v[80:81]
	v_pk_mul_f32 v[94:95], v[94:95], v[98:99]
	v_mul_f32_e32 v80, 0x4038aa3b, v82
	v_mul_f32_e32 v81, 0x4038aa3b, v83
	v_mul_f32_e32 v98, 0x4038aa3b, v96
	v_mul_f32_e32 v99, 0x4038aa3b, v97
	v_fmamk_f32 v84, v84, 0xbfb8aa3b, v146
	v_fmamk_f32 v85, v85, 0xbfb8aa3b, v147
	v_fmamk_f32 v86, v86, 0xbfb8aa3b, v144
	v_fmamk_f32 v87, v87, 0xbfb8aa3b, v145
	v_exp_f32_e32 v99, v99
	v_exp_f32_e32 v98, v98
	v_exp_f32_e32 v81, v81
	v_exp_f32_e32 v80, v80
	v_exp_f32_e32 v84, v84
	v_exp_f32_e32 v86, v86
	v_exp_f32_e32 v87, v87
	v_exp_f32_e32 v85, v85
	v_sub_f32_e32 v99, 1.0, v99
	v_sub_f32_e32 v98, 1.0, v98
	v_sub_f32_e32 v81, 1.0, v81
	v_sub_f32_e32 v80, 1.0, v80
	v_pk_add_f32 v[86:87], v[86:87], 1.0 op_sel_hi:[1,0]
	v_pk_add_f32 v[84:85], v[84:85], 1.0 op_sel_hi:[1,0]
	v_max_f32_e32 v80, 0, v80
	v_max_f32_e32 v81, 0, v81
	v_max_f32_e32 v98, 0, v98
	v_max_f32_e32 v99, 0, v99
	v_rcp_f32_e32 v84, v84
	v_rcp_f32_e32 v85, v85
	v_rcp_f32_e32 v86, v86
	v_rcp_f32_e32 v87, v87
	v_sqrt_f32_e32 v80, v80
	v_sqrt_f32_e32 v81, v81
	v_sqrt_f32_e32 v98, v98
	v_sqrt_f32_e32 v99, v99
	s_waitcnt vmcnt(2)
	v_lshlrev_b32_e32 v100, 16, v104
	v_and_b32_e32 v101, 0xffff0000, v104
	v_lshlrev_b32_e32 v102, 16, v105
	v_and_b32_e32 v103, 0xffff0000, v105
	v_pk_mul_f32 v[94:95], v[94:95], v[102:103]
	v_pk_mul_f32 v[92:93], v[92:93], v[100:101]
	v_lshlrev_b32_e32 v100, 16, v106
	v_and_b32_e32 v101, 0xffff0000, v106
	v_lshlrev_b32_e32 v102, 16, v107
	v_and_b32_e32 v103, 0xffff0000, v107
	v_pk_mul_f32 v[86:87], v[86:87], v[98:99]
	v_pk_mul_f32 v[80:81], v[84:85], v[80:81]
	v_pk_mul_f32 v[98:99], v[86:87], v[102:103]
	v_pk_mul_f32 v[86:87], v[80:81], v[100:101]
	v_cvt_pk_bf16_f32 v80, v88, v89
	v_cvt_pk_bf16_f32 v81, v90, v91
	v_cvt_pk_bf16_f32 v82, v82, v83
	v_cvt_pk_bf16_f32 v83, v96, v97
	v_cvt_pk_bf16_f32 v84, v92, v93
	v_or_b32_e32 v92, 48, v152
	v_ashrrev_i32_e32 v93, 31, v92
	v_lshlrev_b64 v[88:89], 11, v[92:93]
	v_lshl_add_u64 v[88:89], s[10:11], 0, v[88:89]
	v_cvt_pk_bf16_f32 v85, v94, v95
	v_cvt_pk_bf16_f32 v86, v86, v87
	v_cvt_pk_bf16_f32 v87, v98, v99
	v_lshl_add_u64 v[88:89], v[88:89], 0, v[154:155]
	v_mov_b64_e32 v[88:89], v[204:205]
	v_mov_b64_e32 v[90:91], v[206:207]
	v_fmamk_f32 v72, v72, 0xbfb8aa3b, v150
	v_fmamk_f32 v73, v73, 0xbfb8aa3b, v151
	v_exp_f32_e32 v72, v72
	v_exp_f32_e32 v73, v73
	v_fmamk_f32 v74, v74, 0xbfb8aa3b, v148
	v_fmamk_f32 v75, v75, 0xbfb8aa3b, v149
	v_exp_f32_e32 v74, v74
	v_exp_f32_e32 v75, v75
	v_pk_add_f32 v[72:73], v[72:73], 1.0 op_sel_hi:[1,0]
	v_lshlrev_b64 v[94:95], 10, v[108:109]
	v_rcp_f32_e32 v72, v72
	v_pk_add_f32 v[74:75], v[74:75], 1.0 op_sel_hi:[1,0]
	v_rcp_f32_e32 v73, v73
	v_lshl_add_u64 v[94:95], v[94:95], 0, v[160:161]
	v_rcp_f32_e32 v74, v74
	v_rcp_f32_e32 v75, v75
	v_lshlrev_b64 v[94:95], 1, v[94:95]
	v_lshl_add_u64 v[96:97], s[44:45], 0, v[94:95]
	global_store_dwordx4 v[96:97], v[80:83], off
	v_pk_mul_f32 v[72:73], v[120:121], v[72:73]
	v_pk_mul_f32 v[74:75], v[122:123], v[74:75]
	v_lshl_add_u64 v[80:81], s[46:47], 0, v[94:95]
	global_store_dwordx4 v[80:81], v[84:87], off
	v_mul_f32_e32 v80, 0x4038aa3b, v72
	v_mul_f32_e32 v81, 0x4038aa3b, v73
	v_fmamk_f32 v76, v76, 0xbfb8aa3b, v158
	v_fmamk_f32 v77, v77, 0xbfb8aa3b, v159
	v_mul_f32_e32 v82, 0x4038aa3b, v74
	v_mul_f32_e32 v83, 0x4038aa3b, v75
	v_exp_f32_e32 v81, v81
	v_exp_f32_e32 v80, v80
	v_fmamk_f32 v64, v64, 0xbfb8aa3b, v142
	v_fmamk_f32 v65, v65, 0xbfb8aa3b, v143
	v_fmamk_f32 v66, v66, 0xbfb8aa3b, v140
	v_fmamk_f32 v67, v67, 0xbfb8aa3b, v141
	v_exp_f32_e32 v76, v76
	v_fmamk_f32 v78, v78, 0xbfb8aa3b, v156
	v_fmamk_f32 v79, v79, 0xbfb8aa3b, v157
	v_exp_f32_e32 v77, v77
	v_exp_f32_e32 v83, v83
	v_exp_f32_e32 v82, v82
	v_exp_f32_e32 v64, v64
	v_exp_f32_e32 v65, v65
	v_exp_f32_e32 v66, v66
	v_exp_f32_e32 v67, v67
	v_exp_f32_e32 v78, v78
	v_exp_f32_e32 v79, v79
	v_sub_f32_e32 v81, 1.0, v81
	v_sub_f32_e32 v80, 1.0, v80
	v_pk_add_f32 v[76:77], v[76:77], 1.0 op_sel_hi:[1,0]
	v_sub_f32_e32 v83, 1.0, v83
	v_sub_f32_e32 v82, 1.0, v82
	v_max_f32_e32 v80, 0, v80
	v_max_f32_e32 v81, 0, v81
	v_pk_add_f32 v[66:67], v[66:67], 1.0 op_sel_hi:[1,0]
	v_pk_add_f32 v[64:65], v[64:65], 1.0 op_sel_hi:[1,0]
	v_pk_add_f32 v[78:79], v[78:79], 1.0 op_sel_hi:[1,0]
	v_rcp_f32_e32 v76, v76
	v_rcp_f32_e32 v77, v77
	v_sqrt_f32_e32 v80, v80
	v_sqrt_f32_e32 v81, v81
	v_max_f32_e32 v82, 0, v82
	v_max_f32_e32 v83, 0, v83
	v_rcp_f32_e32 v64, v64
	v_rcp_f32_e32 v65, v65
	v_rcp_f32_e32 v66, v66
	v_rcp_f32_e32 v67, v67
	v_rcp_f32_e32 v78, v78
	v_rcp_f32_e32 v79, v79
	v_sqrt_f32_e32 v82, v82
	v_sqrt_f32_e32 v83, v83
	v_pk_mul_f32 v[76:77], v[76:77], v[80:81]
	v_pk_mul_f32 v[80:81], v[112:113], v[66:67]
	v_pk_mul_f32 v[66:67], v[116:117], v[64:65]
	v_pk_mul_f32 v[78:79], v[78:79], v[82:83]
	v_mul_f32_e32 v64, 0x4038aa3b, v66
	v_mul_f32_e32 v65, 0x4038aa3b, v67
	v_mul_f32_e32 v82, 0x4038aa3b, v80
	v_mul_f32_e32 v83, 0x4038aa3b, v81
	v_fmamk_f32 v68, v68, 0xbfb8aa3b, v146
	v_fmamk_f32 v69, v69, 0xbfb8aa3b, v147
	v_fmamk_f32 v70, v70, 0xbfb8aa3b, v144
	v_fmamk_f32 v71, v71, 0xbfb8aa3b, v145
	v_exp_f32_e32 v83, v83
	v_exp_f32_e32 v82, v82
	v_exp_f32_e32 v65, v65
	v_exp_f32_e32 v64, v64
	v_exp_f32_e32 v68, v68
	v_exp_f32_e32 v70, v70
	v_exp_f32_e32 v71, v71
	v_exp_f32_e32 v69, v69
	v_sub_f32_e32 v83, 1.0, v83
	v_sub_f32_e32 v82, 1.0, v82
	v_sub_f32_e32 v65, 1.0, v65
	v_sub_f32_e32 v64, 1.0, v64
	v_pk_add_f32 v[70:71], v[70:71], 1.0 op_sel_hi:[1,0]
	v_pk_add_f32 v[68:69], v[68:69], 1.0 op_sel_hi:[1,0]
	v_max_f32_e32 v64, 0, v64
	v_max_f32_e32 v65, 0, v65
	v_max_f32_e32 v82, 0, v82
	v_max_f32_e32 v83, 0, v83
	v_rcp_f32_e32 v68, v68
	v_rcp_f32_e32 v69, v69
	v_rcp_f32_e32 v70, v70
	v_rcp_f32_e32 v71, v71
	v_sqrt_f32_e32 v64, v64
	v_sqrt_f32_e32 v65, v65
	v_sqrt_f32_e32 v82, v82
	v_sqrt_f32_e32 v83, v83
	s_waitcnt vmcnt(2)
	v_lshlrev_b32_e32 v84, 16, v88
	v_and_b32_e32 v85, 0xffff0000, v88
	v_lshlrev_b32_e32 v86, 16, v89
	v_and_b32_e32 v87, 0xffff0000, v89
	v_pk_mul_f32 v[78:79], v[78:79], v[86:87]
	v_pk_mul_f32 v[76:77], v[76:77], v[84:85]
	v_lshlrev_b32_e32 v84, 16, v90
	v_and_b32_e32 v85, 0xffff0000, v90
	v_lshlrev_b32_e32 v86, 16, v91
	v_and_b32_e32 v87, 0xffff0000, v91
	v_pk_mul_f32 v[70:71], v[70:71], v[82:83]
	v_pk_mul_f32 v[64:65], v[68:69], v[64:65]
	v_pk_mul_f32 v[82:83], v[70:71], v[86:87]
	v_pk_mul_f32 v[70:71], v[64:65], v[84:85]
	v_cvt_pk_bf16_f32 v64, v72, v73
	v_cvt_pk_bf16_f32 v65, v74, v75
	v_cvt_pk_bf16_f32 v66, v66, v67
	v_cvt_pk_bf16_f32 v67, v80, v81
	v_cvt_pk_bf16_f32 v68, v76, v77
	v_add_u32_e32 v76, 0x80, v152
	v_ashrrev_i32_e32 v77, 31, v76
	v_lshlrev_b64 v[72:73], 11, v[76:77]
	v_lshl_add_u64 v[72:73], s[10:11], 0, v[72:73]
	v_cvt_pk_bf16_f32 v69, v78, v79
	v_cvt_pk_bf16_f32 v70, v70, v71
	v_cvt_pk_bf16_f32 v71, v82, v83
	v_lshl_add_u64 v[72:73], v[72:73], 0, v[154:155]
	v_mov_b64_e32 v[72:73], v[208:209]
	v_mov_b64_e32 v[74:75], v[210:211]
	v_fmamk_f32 v56, v56, 0xbfb8aa3b, v150
	v_fmamk_f32 v57, v57, 0xbfb8aa3b, v151
	v_exp_f32_e32 v56, v56
	v_exp_f32_e32 v57, v57
	v_fmamk_f32 v58, v58, 0xbfb8aa3b, v148
	v_fmamk_f32 v59, v59, 0xbfb8aa3b, v149
	v_exp_f32_e32 v58, v58
	v_exp_f32_e32 v59, v59
	v_pk_add_f32 v[56:57], v[56:57], 1.0 op_sel_hi:[1,0]
	v_lshlrev_b64 v[78:79], 10, v[92:93]
	v_rcp_f32_e32 v56, v56
	v_pk_add_f32 v[58:59], v[58:59], 1.0 op_sel_hi:[1,0]
	v_rcp_f32_e32 v57, v57
	v_lshl_add_u64 v[78:79], v[78:79], 0, v[160:161]
	v_rcp_f32_e32 v58, v58
	v_rcp_f32_e32 v59, v59
	v_lshlrev_b64 v[78:79], 1, v[78:79]
	v_lshl_add_u64 v[80:81], s[44:45], 0, v[78:79]
	global_store_dwordx4 v[80:81], v[64:67], off
	v_pk_mul_f32 v[56:57], v[120:121], v[56:57]
	v_pk_mul_f32 v[58:59], v[122:123], v[58:59]
	v_lshl_add_u64 v[64:65], s[46:47], 0, v[78:79]
	global_store_dwordx4 v[64:65], v[68:71], off
	v_mul_f32_e32 v64, 0x4038aa3b, v56
	v_mul_f32_e32 v65, 0x4038aa3b, v57
	v_fmamk_f32 v60, v60, 0xbfb8aa3b, v158
	v_fmamk_f32 v61, v61, 0xbfb8aa3b, v159
	v_mul_f32_e32 v66, 0x4038aa3b, v58
	v_mul_f32_e32 v67, 0x4038aa3b, v59
	v_exp_f32_e32 v65, v65
	v_exp_f32_e32 v64, v64
	v_fmamk_f32 v48, v48, 0xbfb8aa3b, v142
	v_fmamk_f32 v49, v49, 0xbfb8aa3b, v143
	v_fmamk_f32 v50, v50, 0xbfb8aa3b, v140
	v_fmamk_f32 v51, v51, 0xbfb8aa3b, v141
	v_exp_f32_e32 v60, v60
	v_fmamk_f32 v62, v62, 0xbfb8aa3b, v156
	v_fmamk_f32 v63, v63, 0xbfb8aa3b, v157
	v_exp_f32_e32 v61, v61
	v_exp_f32_e32 v67, v67
	v_exp_f32_e32 v66, v66
	v_exp_f32_e32 v48, v48
	v_exp_f32_e32 v49, v49
	v_exp_f32_e32 v50, v50
	v_exp_f32_e32 v51, v51
	v_exp_f32_e32 v62, v62
	v_exp_f32_e32 v63, v63
	v_sub_f32_e32 v65, 1.0, v65
	v_sub_f32_e32 v64, 1.0, v64
	v_pk_add_f32 v[60:61], v[60:61], 1.0 op_sel_hi:[1,0]
	v_sub_f32_e32 v67, 1.0, v67
	v_sub_f32_e32 v66, 1.0, v66
	v_max_f32_e32 v64, 0, v64
	v_max_f32_e32 v65, 0, v65
	v_pk_add_f32 v[50:51], v[50:51], 1.0 op_sel_hi:[1,0]
	v_pk_add_f32 v[48:49], v[48:49], 1.0 op_sel_hi:[1,0]
	v_pk_add_f32 v[62:63], v[62:63], 1.0 op_sel_hi:[1,0]
	v_rcp_f32_e32 v60, v60
	v_rcp_f32_e32 v61, v61
	v_sqrt_f32_e32 v64, v64
	v_sqrt_f32_e32 v65, v65
	v_max_f32_e32 v66, 0, v66
	v_max_f32_e32 v67, 0, v67
	v_rcp_f32_e32 v48, v48
	v_rcp_f32_e32 v49, v49
	v_rcp_f32_e32 v50, v50
	v_rcp_f32_e32 v51, v51
	v_rcp_f32_e32 v62, v62
	v_rcp_f32_e32 v63, v63
	v_sqrt_f32_e32 v66, v66
	v_sqrt_f32_e32 v67, v67
	v_pk_mul_f32 v[60:61], v[60:61], v[64:65]
	v_pk_mul_f32 v[64:65], v[112:113], v[50:51]
	v_pk_mul_f32 v[50:51], v[116:117], v[48:49]
	v_pk_mul_f32 v[62:63], v[62:63], v[66:67]
	v_mul_f32_e32 v48, 0x4038aa3b, v50
	v_mul_f32_e32 v49, 0x4038aa3b, v51
	v_mul_f32_e32 v66, 0x4038aa3b, v64
	v_mul_f32_e32 v67, 0x4038aa3b, v65
	v_fmamk_f32 v52, v52, 0xbfb8aa3b, v146
	v_fmamk_f32 v53, v53, 0xbfb8aa3b, v147
	v_fmamk_f32 v54, v54, 0xbfb8aa3b, v144
	v_fmamk_f32 v55, v55, 0xbfb8aa3b, v145
	v_exp_f32_e32 v67, v67
	v_exp_f32_e32 v66, v66
	v_exp_f32_e32 v49, v49
	v_exp_f32_e32 v48, v48
	v_exp_f32_e32 v52, v52
	v_exp_f32_e32 v54, v54
	v_exp_f32_e32 v55, v55
	v_exp_f32_e32 v53, v53
	v_sub_f32_e32 v67, 1.0, v67
	v_sub_f32_e32 v66, 1.0, v66
	v_sub_f32_e32 v49, 1.0, v49
	v_sub_f32_e32 v48, 1.0, v48
	v_pk_add_f32 v[54:55], v[54:55], 1.0 op_sel_hi:[1,0]
	v_pk_add_f32 v[52:53], v[52:53], 1.0 op_sel_hi:[1,0]
	v_max_f32_e32 v48, 0, v48
	v_max_f32_e32 v49, 0, v49
	v_max_f32_e32 v66, 0, v66
	v_max_f32_e32 v67, 0, v67
	v_rcp_f32_e32 v52, v52
	v_rcp_f32_e32 v53, v53
	v_rcp_f32_e32 v54, v54
	v_rcp_f32_e32 v55, v55
	v_sqrt_f32_e32 v48, v48
	v_sqrt_f32_e32 v49, v49
	v_sqrt_f32_e32 v66, v66
	v_sqrt_f32_e32 v67, v67
	s_waitcnt vmcnt(2)
	v_lshlrev_b32_e32 v68, 16, v72
	v_and_b32_e32 v69, 0xffff0000, v72
	v_lshlrev_b32_e32 v70, 16, v73
	v_and_b32_e32 v71, 0xffff0000, v73
	v_pk_mul_f32 v[62:63], v[62:63], v[70:71]
	v_pk_mul_f32 v[60:61], v[60:61], v[68:69]
	v_lshlrev_b32_e32 v68, 16, v74
	v_and_b32_e32 v69, 0xffff0000, v74
	v_lshlrev_b32_e32 v70, 16, v75
	v_and_b32_e32 v71, 0xffff0000, v75
	v_pk_mul_f32 v[54:55], v[54:55], v[66:67]
	v_pk_mul_f32 v[48:49], v[52:53], v[48:49]
	v_pk_mul_f32 v[66:67], v[54:55], v[70:71]
	v_pk_mul_f32 v[54:55], v[48:49], v[68:69]
	v_cvt_pk_bf16_f32 v48, v56, v57
	v_add_u32_e32 v56, 0x90, v152
	v_ashrrev_i32_e32 v57, 31, v56
	v_lshlrev_b64 v[56:57], 11, v[56:57]
	v_lshl_add_u64 v[56:57], s[10:11], 0, v[56:57]
	v_cvt_pk_bf16_f32 v49, v58, v59
	v_cvt_pk_bf16_f32 v50, v50, v51
	v_cvt_pk_bf16_f32 v51, v64, v65
	v_cvt_pk_bf16_f32 v52, v60, v61
	v_cvt_pk_bf16_f32 v53, v62, v63
	v_cvt_pk_bf16_f32 v54, v54, v55
	v_cvt_pk_bf16_f32 v55, v66, v67
	v_lshl_add_u64 v[56:57], v[56:57], 0, v[154:155]
	v_mov_b64_e32 v[56:57], v[212:213]
	v_mov_b64_e32 v[58:59], v[214:215]
	v_fmamk_f32 v40, v40, 0xbfb8aa3b, v150
	v_fmamk_f32 v41, v41, 0xbfb8aa3b, v151
	v_exp_f32_e32 v40, v40
	v_exp_f32_e32 v41, v41
	v_fmamk_f32 v42, v42, 0xbfb8aa3b, v148
	v_fmamk_f32 v43, v43, 0xbfb8aa3b, v149
	v_exp_f32_e32 v42, v42
	v_exp_f32_e32 v43, v43
	v_pk_add_f32 v[40:41], v[40:41], 1.0 op_sel_hi:[1,0]
	v_lshlrev_b64 v[60:61], 10, v[76:77]
	v_rcp_f32_e32 v40, v40
	v_pk_add_f32 v[42:43], v[42:43], 1.0 op_sel_hi:[1,0]
	v_rcp_f32_e32 v41, v41
	v_lshl_add_u64 v[60:61], v[60:61], 0, v[160:161]
	v_rcp_f32_e32 v42, v42
	v_rcp_f32_e32 v43, v43
	v_lshlrev_b64 v[60:61], 1, v[60:61]
	v_lshl_add_u64 v[62:63], s[44:45], 0, v[60:61]
	global_store_dwordx4 v[62:63], v[48:51], off
	v_pk_mul_f32 v[40:41], v[120:121], v[40:41]
	v_pk_mul_f32 v[42:43], v[122:123], v[42:43]
	v_lshl_add_u64 v[48:49], s[46:47], 0, v[60:61]
	global_store_dwordx4 v[48:49], v[52:55], off
	v_mul_f32_e32 v48, 0x4038aa3b, v40
	v_mul_f32_e32 v49, 0x4038aa3b, v41
	v_fmamk_f32 v44, v44, 0xbfb8aa3b, v158
	v_fmamk_f32 v45, v45, 0xbfb8aa3b, v159
	v_mul_f32_e32 v50, 0x4038aa3b, v42
	v_mul_f32_e32 v51, 0x4038aa3b, v43
	v_exp_f32_e32 v49, v49
	v_exp_f32_e32 v48, v48
	v_fmamk_f32 v32, v32, 0xbfb8aa3b, v142
	v_fmamk_f32 v33, v33, 0xbfb8aa3b, v143
	v_fmamk_f32 v34, v34, 0xbfb8aa3b, v140
	v_fmamk_f32 v35, v35, 0xbfb8aa3b, v141
	v_exp_f32_e32 v44, v44
	v_fmamk_f32 v46, v46, 0xbfb8aa3b, v156
	v_fmamk_f32 v47, v47, 0xbfb8aa3b, v157
	v_exp_f32_e32 v45, v45
	v_exp_f32_e32 v51, v51
	v_exp_f32_e32 v50, v50
	v_exp_f32_e32 v32, v32
	v_exp_f32_e32 v33, v33
	v_exp_f32_e32 v34, v34
	v_exp_f32_e32 v35, v35
	v_exp_f32_e32 v46, v46
	v_exp_f32_e32 v47, v47
	v_sub_f32_e32 v49, 1.0, v49
	v_sub_f32_e32 v48, 1.0, v48
	v_pk_add_f32 v[44:45], v[44:45], 1.0 op_sel_hi:[1,0]
	v_sub_f32_e32 v51, 1.0, v51
	v_sub_f32_e32 v50, 1.0, v50
	v_max_f32_e32 v48, 0, v48
	v_max_f32_e32 v49, 0, v49
	v_pk_add_f32 v[34:35], v[34:35], 1.0 op_sel_hi:[1,0]
	v_pk_add_f32 v[32:33], v[32:33], 1.0 op_sel_hi:[1,0]
	v_pk_add_f32 v[46:47], v[46:47], 1.0 op_sel_hi:[1,0]
	v_rcp_f32_e32 v44, v44
	v_rcp_f32_e32 v45, v45
	v_sqrt_f32_e32 v48, v48
	v_sqrt_f32_e32 v49, v49
	v_max_f32_e32 v50, 0, v50
	v_max_f32_e32 v51, 0, v51
	v_rcp_f32_e32 v32, v32
	v_rcp_f32_e32 v33, v33
	v_rcp_f32_e32 v34, v34
	v_rcp_f32_e32 v35, v35
	v_rcp_f32_e32 v46, v46
	v_rcp_f32_e32 v47, v47
	v_sqrt_f32_e32 v50, v50
	v_sqrt_f32_e32 v51, v51
	v_pk_mul_f32 v[44:45], v[44:45], v[48:49]
	v_pk_mul_f32 v[48:49], v[112:113], v[34:35]
	v_pk_mul_f32 v[34:35], v[116:117], v[32:33]
	v_pk_mul_f32 v[46:47], v[46:47], v[50:51]
	v_mul_f32_e32 v32, 0x4038aa3b, v34
	v_mul_f32_e32 v33, 0x4038aa3b, v35
	v_mul_f32_e32 v50, 0x4038aa3b, v48
	v_mul_f32_e32 v51, 0x4038aa3b, v49
	v_fmamk_f32 v36, v36, 0xbfb8aa3b, v146
	v_fmamk_f32 v37, v37, 0xbfb8aa3b, v147
	v_fmamk_f32 v38, v38, 0xbfb8aa3b, v144
	v_fmamk_f32 v39, v39, 0xbfb8aa3b, v145
	v_exp_f32_e32 v51, v51
	v_exp_f32_e32 v50, v50
	v_exp_f32_e32 v33, v33
	v_exp_f32_e32 v32, v32
	v_exp_f32_e32 v36, v36
	v_exp_f32_e32 v38, v38
	v_exp_f32_e32 v39, v39
	v_exp_f32_e32 v37, v37
	v_sub_f32_e32 v51, 1.0, v51
	v_sub_f32_e32 v50, 1.0, v50
	v_sub_f32_e32 v33, 1.0, v33
	v_sub_f32_e32 v32, 1.0, v32
	v_pk_add_f32 v[38:39], v[38:39], 1.0 op_sel_hi:[1,0]
	v_pk_add_f32 v[36:37], v[36:37], 1.0 op_sel_hi:[1,0]
	v_max_f32_e32 v32, 0, v32
	v_max_f32_e32 v33, 0, v33
	v_max_f32_e32 v50, 0, v50
	v_max_f32_e32 v51, 0, v51
	v_rcp_f32_e32 v36, v36
	v_rcp_f32_e32 v37, v37
	v_rcp_f32_e32 v38, v38
	v_rcp_f32_e32 v39, v39
	v_sqrt_f32_e32 v32, v32
	v_sqrt_f32_e32 v33, v33
	v_sqrt_f32_e32 v50, v50
	v_sqrt_f32_e32 v51, v51
	s_waitcnt vmcnt(2)
	v_lshlrev_b32_e32 v52, 16, v56
	v_and_b32_e32 v53, 0xffff0000, v56
	v_lshlrev_b32_e32 v54, 16, v57
	v_and_b32_e32 v55, 0xffff0000, v57
	v_pk_mul_f32 v[46:47], v[46:47], v[54:55]
	v_pk_mul_f32 v[44:45], v[44:45], v[52:53]
	v_lshlrev_b32_e32 v52, 16, v58
	v_and_b32_e32 v53, 0xffff0000, v58
	v_lshlrev_b32_e32 v54, 16, v59
	v_and_b32_e32 v55, 0xffff0000, v59
	v_pk_mul_f32 v[38:39], v[38:39], v[50:51]
	v_pk_mul_f32 v[32:33], v[36:37], v[32:33]
	v_pk_mul_f32 v[50:51], v[38:39], v[54:55]
	v_pk_mul_f32 v[38:39], v[32:33], v[52:53]
	v_cvt_pk_bf16_f32 v32, v40, v41
	v_add_u32_e32 v40, 0xa0, v152
	v_ashrrev_i32_e32 v41, 31, v40
	v_lshlrev_b64 v[40:41], 11, v[40:41]
	v_lshl_add_u64 v[40:41], s[10:11], 0, v[40:41]
	v_cvt_pk_bf16_f32 v33, v42, v43
	v_cvt_pk_bf16_f32 v34, v34, v35
	v_cvt_pk_bf16_f32 v35, v48, v49
	v_cvt_pk_bf16_f32 v36, v44, v45
	v_cvt_pk_bf16_f32 v37, v46, v47
	v_cvt_pk_bf16_f32 v38, v38, v39
	v_cvt_pk_bf16_f32 v39, v50, v51
	v_lshl_add_u64 v[40:41], v[40:41], 0, v[154:155]
	v_mov_b64_e32 v[40:41], v[216:217]
	v_mov_b64_e32 v[42:43], v[218:219]
	v_fmamk_f32 v24, v24, 0xbfb8aa3b, v150
	v_fmamk_f32 v25, v25, 0xbfb8aa3b, v151
	v_exp_f32_e32 v24, v24
	v_exp_f32_e32 v25, v25
	v_fmamk_f32 v26, v26, 0xbfb8aa3b, v148
	v_fmamk_f32 v27, v27, 0xbfb8aa3b, v149
	v_exp_f32_e32 v26, v26
	v_exp_f32_e32 v27, v27
	v_pk_add_f32 v[24:25], v[24:25], 1.0 op_sel_hi:[1,0]
	v_lshl_add_u64 v[44:45], v[114:115], 0, s[28:29]
	v_rcp_f32_e32 v24, v24
	v_pk_add_f32 v[26:27], v[26:27], 1.0 op_sel_hi:[1,0]
	v_rcp_f32_e32 v25, v25
	v_rcp_f32_e32 v26, v26
	v_rcp_f32_e32 v27, v27
	v_lshl_add_u64 v[46:47], s[44:45], 0, v[44:45]
	global_store_dwordx4 v[46:47], v[32:35], off
	v_pk_mul_f32 v[24:25], v[120:121], v[24:25]
	v_pk_mul_f32 v[26:27], v[122:123], v[26:27]
	v_lshl_add_u64 v[32:33], s[46:47], 0, v[44:45]
	global_store_dwordx4 v[32:33], v[36:39], off
	v_mul_f32_e32 v32, 0x4038aa3b, v24
	v_mul_f32_e32 v33, 0x4038aa3b, v25
	v_fmamk_f32 v28, v28, 0xbfb8aa3b, v158
	v_fmamk_f32 v29, v29, 0xbfb8aa3b, v159
	v_mul_f32_e32 v34, 0x4038aa3b, v26
	v_mul_f32_e32 v35, 0x4038aa3b, v27
	v_exp_f32_e32 v33, v33
	v_exp_f32_e32 v32, v32
	v_fmamk_f32 v16, v16, 0xbfb8aa3b, v142
	v_fmamk_f32 v17, v17, 0xbfb8aa3b, v143
	v_fmamk_f32 v18, v18, 0xbfb8aa3b, v140
	v_fmamk_f32 v19, v19, 0xbfb8aa3b, v141
	v_exp_f32_e32 v28, v28
	v_fmamk_f32 v30, v30, 0xbfb8aa3b, v156
	v_fmamk_f32 v31, v31, 0xbfb8aa3b, v157
	v_exp_f32_e32 v29, v29
	v_exp_f32_e32 v35, v35
	v_exp_f32_e32 v34, v34
	v_exp_f32_e32 v16, v16
	v_exp_f32_e32 v17, v17
	v_exp_f32_e32 v18, v18
	v_exp_f32_e32 v19, v19
	v_exp_f32_e32 v30, v30
	v_exp_f32_e32 v31, v31
	v_sub_f32_e32 v33, 1.0, v33
	v_sub_f32_e32 v32, 1.0, v32
	v_pk_add_f32 v[28:29], v[28:29], 1.0 op_sel_hi:[1,0]
	v_sub_f32_e32 v35, 1.0, v35
	v_sub_f32_e32 v34, 1.0, v34
	v_max_f32_e32 v32, 0, v32
	v_max_f32_e32 v33, 0, v33
	v_pk_add_f32 v[18:19], v[18:19], 1.0 op_sel_hi:[1,0]
	v_pk_add_f32 v[16:17], v[16:17], 1.0 op_sel_hi:[1,0]
	v_pk_add_f32 v[30:31], v[30:31], 1.0 op_sel_hi:[1,0]
	v_rcp_f32_e32 v28, v28
	v_rcp_f32_e32 v29, v29
	v_sqrt_f32_e32 v32, v32
	v_sqrt_f32_e32 v33, v33
	v_max_f32_e32 v34, 0, v34
	v_max_f32_e32 v35, 0, v35
	v_rcp_f32_e32 v16, v16
	v_rcp_f32_e32 v17, v17
	v_rcp_f32_e32 v18, v18
	v_rcp_f32_e32 v19, v19
	v_rcp_f32_e32 v30, v30
	v_rcp_f32_e32 v31, v31
	v_sqrt_f32_e32 v34, v34
	v_sqrt_f32_e32 v35, v35
	v_pk_mul_f32 v[28:29], v[28:29], v[32:33]
	v_pk_mul_f32 v[32:33], v[112:113], v[18:19]
	v_pk_mul_f32 v[18:19], v[116:117], v[16:17]
	v_pk_mul_f32 v[30:31], v[30:31], v[34:35]
	v_mul_f32_e32 v16, 0x4038aa3b, v18
	v_mul_f32_e32 v17, 0x4038aa3b, v19
	v_mul_f32_e32 v34, 0x4038aa3b, v32
	v_mul_f32_e32 v35, 0x4038aa3b, v33
	v_fmamk_f32 v20, v20, 0xbfb8aa3b, v146
	v_fmamk_f32 v21, v21, 0xbfb8aa3b, v147
	v_fmamk_f32 v22, v22, 0xbfb8aa3b, v144
	v_fmamk_f32 v23, v23, 0xbfb8aa3b, v145
	v_exp_f32_e32 v35, v35
	v_exp_f32_e32 v34, v34
	v_exp_f32_e32 v17, v17
	v_exp_f32_e32 v16, v16
	v_exp_f32_e32 v20, v20
	v_exp_f32_e32 v22, v22
	v_exp_f32_e32 v23, v23
	v_exp_f32_e32 v21, v21
	v_sub_f32_e32 v35, 1.0, v35
	v_sub_f32_e32 v34, 1.0, v34
	v_sub_f32_e32 v17, 1.0, v17
	v_sub_f32_e32 v16, 1.0, v16
	v_pk_add_f32 v[22:23], v[22:23], 1.0 op_sel_hi:[1,0]
	v_pk_add_f32 v[20:21], v[20:21], 1.0 op_sel_hi:[1,0]
	v_max_f32_e32 v16, 0, v16
	v_max_f32_e32 v17, 0, v17
	v_max_f32_e32 v34, 0, v34
	v_max_f32_e32 v35, 0, v35
	v_rcp_f32_e32 v20, v20
	v_rcp_f32_e32 v21, v21
	v_rcp_f32_e32 v22, v22
	v_rcp_f32_e32 v23, v23
	v_sqrt_f32_e32 v16, v16
	v_sqrt_f32_e32 v17, v17
	v_sqrt_f32_e32 v34, v34
	v_sqrt_f32_e32 v35, v35
	s_waitcnt vmcnt(2)
	v_lshlrev_b32_e32 v36, 16, v40
	v_and_b32_e32 v37, 0xffff0000, v40
	v_lshlrev_b32_e32 v38, 16, v41
	v_and_b32_e32 v39, 0xffff0000, v41
	v_pk_mul_f32 v[30:31], v[30:31], v[38:39]
	v_pk_mul_f32 v[28:29], v[28:29], v[36:37]
	v_lshlrev_b32_e32 v36, 16, v42
	v_and_b32_e32 v37, 0xffff0000, v42
	v_lshlrev_b32_e32 v38, 16, v43
	v_and_b32_e32 v39, 0xffff0000, v43
	v_pk_mul_f32 v[22:23], v[22:23], v[34:35]
	v_pk_mul_f32 v[16:17], v[20:21], v[16:17]
	v_pk_mul_f32 v[34:35], v[22:23], v[38:39]
	v_pk_mul_f32 v[22:23], v[16:17], v[36:37]
	v_cvt_pk_bf16_f32 v16, v24, v25
	v_add_u32_e32 v24, 0xb0, v152
	v_ashrrev_i32_e32 v25, 31, v24
	v_lshlrev_b64 v[24:25], 11, v[24:25]
	v_lshl_add_u64 v[24:25], s[10:11], 0, v[24:25]
	v_cvt_pk_bf16_f32 v17, v26, v27
	v_cvt_pk_bf16_f32 v18, v18, v19
	v_cvt_pk_bf16_f32 v19, v32, v33
	v_cvt_pk_bf16_f32 v20, v28, v29
	v_cvt_pk_bf16_f32 v21, v30, v31
	v_cvt_pk_bf16_f32 v22, v22, v23
	v_cvt_pk_bf16_f32 v23, v34, v35
	v_lshl_add_u64 v[24:25], v[24:25], 0, v[154:155]
	v_mov_b64_e32 v[24:25], v[220:221]
	v_mov_b64_e32 v[26:27], v[222:223]
	v_fmamk_f32 v8, v8, 0xbfb8aa3b, v150
	v_fmac_f32_e32 v151, 0xbfb8aa3b, v9
	v_exp_f32_e32 v8, v8
	v_exp_f32_e32 v9, v151
	v_fmamk_f32 v10, v10, 0xbfb8aa3b, v148
	v_fmac_f32_e32 v149, 0xbfb8aa3b, v11
	v_exp_f32_e32 v10, v10
	v_exp_f32_e32 v11, v149
	v_pk_add_f32 v[8:9], v[8:9], 1.0 op_sel_hi:[1,0]
	v_lshl_add_u64 v[28:29], v[114:115], 0, s[30:31]
	v_rcp_f32_e32 v8, v8
	v_pk_add_f32 v[10:11], v[10:11], 1.0 op_sel_hi:[1,0]
	v_rcp_f32_e32 v9, v9
	v_rcp_f32_e32 v10, v10
	v_rcp_f32_e32 v11, v11
	v_lshl_add_u64 v[30:31], s[44:45], 0, v[28:29]
	global_store_dwordx4 v[30:31], v[16:19], off
	v_pk_mul_f32 v[8:9], v[120:121], v[8:9]
	v_pk_mul_f32 v[10:11], v[122:123], v[10:11]
	v_lshl_add_u64 v[16:17], s[46:47], 0, v[28:29]
	global_store_dwordx4 v[16:17], v[20:23], off
	v_mul_f32_e32 v16, 0x4038aa3b, v8
	v_mul_f32_e32 v17, 0x4038aa3b, v9
	v_fmamk_f32 v12, v12, 0xbfb8aa3b, v158
	v_fmac_f32_e32 v159, 0xbfb8aa3b, v13
	v_fmamk_f32 v13, v14, 0xbfb8aa3b, v156
	v_mul_f32_e32 v18, 0x4038aa3b, v10
	v_mul_f32_e32 v19, 0x4038aa3b, v11
	v_exp_f32_e32 v17, v17
	v_exp_f32_e32 v16, v16
	v_fmamk_f32 v0, v0, 0xbfb8aa3b, v142
	v_fmac_f32_e32 v143, 0xbfb8aa3b, v1
	v_fmamk_f32 v2, v2, 0xbfb8aa3b, v140
	v_fmac_f32_e32 v141, 0xbfb8aa3b, v3
	v_exp_f32_e32 v12, v12
	v_exp_f32_e32 v14, v13
	v_fmac_f32_e32 v157, 0xbfb8aa3b, v15
	v_exp_f32_e32 v13, v159
	v_exp_f32_e32 v19, v19
	v_exp_f32_e32 v18, v18
	v_exp_f32_e32 v0, v0
	v_exp_f32_e32 v1, v143
	v_exp_f32_e32 v2, v2
	v_exp_f32_e32 v3, v141
	v_exp_f32_e32 v15, v157
	v_sub_f32_e32 v17, 1.0, v17
	v_sub_f32_e32 v16, 1.0, v16
	v_pk_add_f32 v[12:13], v[12:13], 1.0 op_sel_hi:[1,0]
	v_sub_f32_e32 v19, 1.0, v19
	v_sub_f32_e32 v18, 1.0, v18
	v_max_f32_e32 v16, 0, v16
	v_max_f32_e32 v17, 0, v17
	v_pk_add_f32 v[2:3], v[2:3], 1.0 op_sel_hi:[1,0]
	v_pk_add_f32 v[0:1], v[0:1], 1.0 op_sel_hi:[1,0]
	v_pk_add_f32 v[14:15], v[14:15], 1.0 op_sel_hi:[1,0]
	v_rcp_f32_e32 v12, v12
	v_rcp_f32_e32 v13, v13
	v_sqrt_f32_e32 v16, v16
	v_sqrt_f32_e32 v17, v17
	v_max_f32_e32 v18, 0, v18
	v_max_f32_e32 v19, 0, v19
	v_rcp_f32_e32 v0, v0
	v_rcp_f32_e32 v1, v1
	v_rcp_f32_e32 v2, v2
	v_rcp_f32_e32 v3, v3
	v_rcp_f32_e32 v14, v14
	v_rcp_f32_e32 v15, v15
	v_sqrt_f32_e32 v18, v18
	v_sqrt_f32_e32 v19, v19
	v_pk_mul_f32 v[12:13], v[12:13], v[16:17]
	v_pk_mul_f32 v[16:17], v[112:113], v[2:3]
	v_pk_mul_f32 v[2:3], v[116:117], v[0:1]
	v_pk_mul_f32 v[14:15], v[14:15], v[18:19]
	v_mul_f32_e32 v0, 0x4038aa3b, v2
	v_mul_f32_e32 v1, 0x4038aa3b, v3
	v_mul_f32_e32 v18, 0x4038aa3b, v16
	v_mul_f32_e32 v19, 0x4038aa3b, v17
	v_fmamk_f32 v4, v4, 0xbfb8aa3b, v146
	v_fmac_f32_e32 v147, 0xbfb8aa3b, v5
	v_fmamk_f32 v5, v6, 0xbfb8aa3b, v144
	v_fmac_f32_e32 v145, 0xbfb8aa3b, v7
	v_exp_f32_e32 v19, v19
	v_exp_f32_e32 v18, v18
	v_exp_f32_e32 v1, v1
	v_exp_f32_e32 v0, v0
	v_exp_f32_e32 v4, v4
	v_exp_f32_e32 v6, v5
	v_exp_f32_e32 v7, v145
	v_exp_f32_e32 v5, v147
	v_sub_f32_e32 v19, 1.0, v19
	v_sub_f32_e32 v18, 1.0, v18
	v_sub_f32_e32 v1, 1.0, v1
	v_sub_f32_e32 v0, 1.0, v0
	v_pk_add_f32 v[6:7], v[6:7], 1.0 op_sel_hi:[1,0]
	v_pk_add_f32 v[4:5], v[4:5], 1.0 op_sel_hi:[1,0]
	v_max_f32_e32 v0, 0, v0
	v_max_f32_e32 v1, 0, v1
	v_max_f32_e32 v18, 0, v18
	v_max_f32_e32 v19, 0, v19
	v_rcp_f32_e32 v4, v4
	v_rcp_f32_e32 v5, v5
	v_rcp_f32_e32 v6, v6
	v_rcp_f32_e32 v7, v7
	v_sqrt_f32_e32 v0, v0
	v_sqrt_f32_e32 v1, v1
	v_sqrt_f32_e32 v18, v18
	v_sqrt_f32_e32 v19, v19
	s_waitcnt vmcnt(2)
	v_lshlrev_b32_e32 v20, 16, v24
	v_and_b32_e32 v21, 0xffff0000, v24
	v_lshlrev_b32_e32 v22, 16, v25
	v_and_b32_e32 v23, 0xffff0000, v25
	v_pk_mul_f32 v[14:15], v[14:15], v[22:23]
	v_pk_mul_f32 v[12:13], v[12:13], v[20:21]
	v_lshlrev_b32_e32 v20, 16, v26
	v_and_b32_e32 v21, 0xffff0000, v26
	v_lshlrev_b32_e32 v22, 16, v27
	v_and_b32_e32 v23, 0xffff0000, v27
	v_pk_mul_f32 v[6:7], v[6:7], v[18:19]
	v_pk_mul_f32 v[0:1], v[4:5], v[0:1]
	v_pk_mul_f32 v[18:19], v[6:7], v[22:23]
	v_pk_mul_f32 v[6:7], v[0:1], v[20:21]
	v_cvt_pk_bf16_f32 v0, v8, v9
	v_lshl_add_u64 v[8:9], v[114:115], 0, s[34:35]
	v_cvt_pk_bf16_f32 v1, v10, v11
	v_cvt_pk_bf16_f32 v2, v2, v3
	v_cvt_pk_bf16_f32 v3, v16, v17
	v_cvt_pk_bf16_f32 v4, v12, v13
	v_cvt_pk_bf16_f32 v5, v14, v15
	v_cvt_pk_bf16_f32 v6, v6, v7
	v_cvt_pk_bf16_f32 v7, v18, v19
	v_lshl_add_u64 v[10:11], s[44:45], 0, v[8:9]
	global_store_dwordx4 v[10:11], v[0:3], off
	s_nop 1
	v_lshl_add_u64 v[0:1], s[46:47], 0, v[8:9]
	global_store_dwordx4 v[0:1], v[4:7], off
	s_cbranch_vccnz .LBB0_516
	s_andn2_b64 vcc, exec, s[12:13]
	s_cbranch_vccnz .LBB0_515
	s_barrier
	s_branch .LBB0_515

.LBB0_1906:
	s_cmp_gt_i32 s89, 17
	s_cselect_b64 s[6:7], -1, 0
	s_and_b64 s[2:3], s[2:3], s[6:7]
	s_andn2_b64 vcc, exec, s[2:3]
	s_branch .LBB0_1958
	s_waitcnt vmcnt(0)
	s_cmp_lg_u32 s96, 0
	s_waitcnt vmcnt(0)
	s_barrier
	s_cbranch_scc1 .LBB0_1957
	v_mbcnt_lo_u32_b32 v0, -1, 0
	v_mbcnt_hi_u32_b32 v0, -1, v0
	v_cmp_eq_u32_e32 vcc, 0, v0
	s_and_saveexec_b64 s[2:3], vcc
	s_cbranch_execz .LBB0_1956
	s_add_i32 s4, 0, 0x27e20
	v_mov_b32_e32 v0, s4
	s_waitcnt vmcnt(0) expcnt(0) lgkmcnt(0)
	ds_read_b32 v2, v0
	s_add_i32 s4, 0, 0x27e24
	v_mov_b32_e32 v0, s4
	ds_read_b32 v0, v0
	s_waitcnt lgkmcnt(1)
	v_cmp_ne_u32_e32 vcc, 0, v2
	s_cbranch_vccnz .LBB0_1924
	s_load_dwordx2 s[10:11], s[0:1], 0x108
	s_load_dword s9, s[0:1], 0x110
	s_add_u32 s4, s82, 0x1000
	s_addc_u32 s5, s83, 0
	s_add_u32 s8, s82, 0x1100
	s_waitcnt lgkmcnt(0)
	s_mul_i32 s20, s11, s10
	s_mul_i32 s20, s20, s9
	s_addc_u32 s9, s83, 0
	s_add_u32 s10, s82, 0x1200
	s_addc_u32 s11, s83, 0
	s_add_u32 s12, s82, 0x1300
	s_addc_u32 s13, s83, 0
	s_mov_b32 s21, 1
	v_mov_b32_e32 v16, 0
	s_branch .LBB0_1912

.LBB0_2345:
	s_lshl_b32 s35, s42, 6
	s_lshl_b32 s41, s42, 7
	s_and_b32 s35, s35, 0xffffff00
	s_and_b32 s41, s41, 0x80
	s_bfe_u32 s31, s42, 0x10001
	s_or_b32 s35, s35, s41
	v_add_u32_e32 v160, s35, v164
	s_lshl_b32 s35, s31, 12
	s_add_u32 s42, s58, s35
	v_ashrrev_i32_e32 v161, 31, v160
	s_addc_u32 s43, s59, 0
	v_lshlrev_b64 v[140:141], 2, v[160:161]
	v_lshl_add_u64 v[146:147], s[42:43], 0, v[140:141]
	global_load_dwordx4 v[142:145], v[146:147], off offset:16
	s_nop 0
	global_load_dwordx4 v[146:149], v[146:147], off
	v_lshl_add_u32 v152, s40, 8, v163
	v_ashrrev_i32_e32 v153, 31, v152
	v_lshlrev_b64 v[150:151], 11, v[152:153]
	v_lshl_add_u64 v[150:151], s[6:7], 0, v[150:151]
	v_lshlrev_b64 v[154:155], 1, v[160:161]
	s_add_u32 s40, s60, s35
	v_lshl_add_u64 v[150:151], v[150:151], 0, v[154:155]
	s_addc_u32 s41, s61, 0
	global_load_dwordx4 v[168:171], v[150:151], off
	s_mov_b32 s99, 0
	s_mov_b32 s98, 0x8000
	v_lshl_add_u64 v[224:225], v[150:151], 0, s[98:99]
	global_load_dwordx4 v[196:199], v[224:225], off
	s_mov_b32 s98, 0x10000
	v_lshl_add_u64 v[228:229], v[150:151], 0, s[98:99]
	global_load_dwordx4 v[200:203], v[228:229], off
	s_mov_b32 s98, 0x18000
	v_lshl_add_u64 v[224:225], v[150:151], 0, s[98:99]
	global_load_dwordx4 v[204:207], v[224:225], off
	s_mov_b32 s98, 0x40000
	v_lshl_add_u64 v[228:229], v[150:151], 0, s[98:99]
	global_load_dwordx4 v[208:211], v[228:229], off
	s_mov_b32 s98, 0x48000
	v_lshl_add_u64 v[224:225], v[150:151], 0, s[98:99]
	global_load_dwordx4 v[212:215], v[224:225], off
	s_mov_b32 s98, 0x50000
	v_lshl_add_u64 v[228:229], v[150:151], 0, s[98:99]
	global_load_dwordx4 v[216:219], v[228:229], off
	s_mov_b32 s98, 0x58000
	v_lshl_add_u64 v[224:225], v[150:151], 0, s[98:99]
	global_load_dwordx4 v[220:223], v[224:225], off
	v_lshl_add_u64 v[150:151], s[40:41], 0, v[140:141]
	global_load_dwordx4 v[172:175], v[150:151], off
	global_load_dwordx4 v[176:179], v[150:151], off offset:16
	s_add_u32 s40, s62, s35
	s_addc_u32 s41, s63, 0
	v_lshl_add_u64 v[140:141], s[40:41], 0, v[140:141]
	global_load_dwordx4 v[180:183], v[140:141], off
	global_load_dwordx4 v[184:187], v[140:141], off offset:16
	s_mul_i32 s31, s31, 0x4400000
	s_add_u32 s40, s54, s31
	s_addc_u32 s41, s55, 0
	s_add_u32 s42, s56, s31
	s_addc_u32 s43, s57, 0
	s_andn2_b64 vcc, exec, s[2:3]
	s_mov_b64 s[2:3], -1
	s_waitcnt vmcnt(0)
	v_pk_mul_f32 v[142:143], v[142:143], s[20:21] op_sel_hi:[1,0]
	v_pk_mul_f32 v[148:149], v[148:149], s[20:21] op_sel_hi:[1,0]
	v_pk_mul_f32 v[150:151], v[146:147], s[20:21] op_sel_hi:[1,0]
	v_fmamk_f32 v126, v126, 0xbfb8aa3b, v148
	v_fmamk_f32 v124, v124, 0xbfb8aa3b, v150
	v_fmamk_f32 v125, v125, 0xbfb8aa3b, v151
	v_fmamk_f32 v127, v127, 0xbfb8aa3b, v149
	v_exp_f32_e32 v124, v124
	v_exp_f32_e32 v125, v125
	v_exp_f32_e32 v126, v126
	v_exp_f32_e32 v127, v127
	v_pk_mul_f32 v[158:159], v[172:173], s[20:21] op_sel_hi:[1,0]
	v_pk_mul_f32 v[156:157], v[174:175], s[20:21] op_sel_hi:[1,0]
	v_pk_mul_f32 v[146:147], v[176:177], s[20:21] op_sel_hi:[1,0]
	v_fmamk_f32 v174, v120, 0xbfb8aa3b, v158
	v_fmamk_f32 v176, v121, 0xbfb8aa3b, v159
	v_pk_add_f32 v[126:127], v[126:127], 1.0 op_sel_hi:[1,0]
	v_pk_add_f32 v[124:125], v[124:125], 1.0 op_sel_hi:[1,0]
	v_fmamk_f32 v190, v116, 0xbfb8aa3b, v146
	v_fmamk_f32 v191, v117, 0xbfb8aa3b, v147
	v_exp_f32_e32 v116, v174
	v_exp_f32_e32 v117, v176
	v_rcp_f32_e32 v124, v124
	v_rcp_f32_e32 v125, v125
	v_rcp_f32_e32 v126, v126
	v_rcp_f32_e32 v127, v127
	v_fmamk_f32 v175, v122, 0xbfb8aa3b, v156
	v_fmamk_f32 v177, v123, 0xbfb8aa3b, v157
	v_pk_mul_f32 v[122:123], v[182:183], s[22:23] op_sel_hi:[1,0]
	v_pk_mul_f32 v[120:121], v[180:181], s[22:23] op_sel_hi:[1,0]
	v_pk_add_f32 v[116:117], v[116:117], 1.0 op_sel_hi:[1,0]
	v_pk_mul_f32 v[126:127], v[122:123], v[126:127]
	v_pk_mul_f32 v[124:125], v[120:121], v[124:125]
	v_pk_mul_f32 v[140:141], v[144:145], s[20:21] op_sel_hi:[1,0]
	v_pk_mul_f32 v[144:145], v[178:179], s[20:21] op_sel_hi:[1,0]
	v_fmamk_f32 v112, v112, 0xbfb8aa3b, v142
	v_fmamk_f32 v113, v113, 0xbfb8aa3b, v143
	v_exp_f32_e32 v174, v175
	v_exp_f32_e32 v175, v177
	v_rcp_f32_e32 v176, v116
	v_rcp_f32_e32 v177, v117
	v_mul_f32_e32 v116, 0x4038aa3b, v124
	v_mul_f32_e32 v117, 0x4038aa3b, v125
	v_mul_f32_e32 v178, 0x4038aa3b, v127
	v_fmamk_f32 v114, v114, 0xbfb8aa3b, v140
	v_exp_f32_e32 v172, v112
	v_exp_f32_e32 v173, v113
	v_fmamk_f32 v192, v118, 0xbfb8aa3b, v144
	v_mul_f32_e32 v118, 0x4038aa3b, v126
	v_exp_f32_e32 v178, v178
	v_exp_f32_e32 v117, v117
	v_exp_f32_e32 v116, v116
	v_fmamk_f32 v115, v115, 0xbfb8aa3b, v141
	v_exp_f32_e32 v114, v114
	v_exp_f32_e32 v118, v118
	v_exp_f32_e32 v115, v115
	v_sub_f32_e32 v178, 1.0, v178
	v_sub_f32_e32 v117, 1.0, v117
	v_sub_f32_e32 v116, 1.0, v116
	v_pk_add_f32 v[172:173], v[172:173], 1.0 op_sel_hi:[1,0]
	v_sub_f32_e32 v118, 1.0, v118
	v_max_f32_e32 v116, 0, v116
	v_max_f32_e32 v117, 0, v117
	v_max_f32_e32 v179, 0, v178
	v_pk_add_f32 v[114:115], v[114:115], 1.0 op_sel_hi:[1,0]
	v_rcp_f32_e32 v172, v172
	v_rcp_f32_e32 v173, v173
	v_pk_add_f32 v[174:175], v[174:175], 1.0 op_sel_hi:[1,0]
	v_max_f32_e32 v118, 0, v118
	v_sqrt_f32_e32 v178, v116
	v_sqrt_f32_e32 v181, v179
	v_sqrt_f32_e32 v179, v117
	v_rcp_f32_e32 v114, v114
	v_rcp_f32_e32 v115, v115
	v_rcp_f32_e32 v174, v174
	v_rcp_f32_e32 v175, v175
	v_sqrt_f32_e32 v180, v118
	v_pk_mul_f32 v[116:117], v[184:185], s[22:23] op_sel_hi:[1,0]
	v_pk_mul_f32 v[112:113], v[186:187], s[22:23] op_sel_hi:[1,0]
	v_pk_mul_f32 v[172:173], v[116:117], v[172:173]
	v_pk_mul_f32 v[176:177], v[176:177], v[178:179]
	v_pk_mul_f32 v[114:115], v[112:113], v[114:115]
	v_mul_f32_e32 v178, 0x4038aa3b, v172
	v_mul_f32_e32 v179, 0x4038aa3b, v173
	v_lshlrev_b32_e32 v188, 16, v168
	v_and_b32_e32 v189, 0xffff0000, v168
	v_lshlrev_b32_e32 v168, 16, v169
	v_and_b32_e32 v169, 0xffff0000, v169
	v_pk_mul_f32 v[174:175], v[174:175], v[180:181]
	v_fmamk_f32 v119, v119, 0xbfb8aa3b, v145
	v_mul_f32_e32 v180, 0x4038aa3b, v114
	v_mul_f32_e32 v181, 0x4038aa3b, v115
	v_exp_f32_e32 v179, v179
	v_exp_f32_e32 v178, v178
	v_exp_f32_e32 v118, v190
	v_pk_mul_f32 v[174:175], v[174:175], v[168:169]
	v_pk_mul_f32 v[168:169], v[176:177], v[188:189]
	v_exp_f32_e32 v177, v119
	v_exp_f32_e32 v119, v191
	v_exp_f32_e32 v181, v181
	v_exp_f32_e32 v180, v180
	v_exp_f32_e32 v176, v192
	v_sub_f32_e32 v179, 1.0, v179
	v_sub_f32_e32 v178, 1.0, v178
	v_pk_add_f32 v[118:119], v[118:119], 1.0 op_sel_hi:[1,0]
	v_sub_f32_e32 v181, 1.0, v181
	v_sub_f32_e32 v180, 1.0, v180
	v_max_f32_e32 v178, 0, v178
	v_max_f32_e32 v179, 0, v179
	v_pk_add_f32 v[176:177], v[176:177], 1.0 op_sel_hi:[1,0]
	v_rcp_f32_e32 v118, v118
	v_rcp_f32_e32 v119, v119
	v_sqrt_f32_e32 v178, v178
	v_sqrt_f32_e32 v179, v179
	v_max_f32_e32 v180, 0, v180
	v_max_f32_e32 v181, 0, v181
	v_rcp_f32_e32 v176, v176
	v_rcp_f32_e32 v177, v177
	v_sqrt_f32_e32 v180, v180
	v_sqrt_f32_e32 v181, v181
	v_lshlrev_b32_e32 v182, 16, v170
	v_and_b32_e32 v183, 0xffff0000, v170
	v_pk_mul_f32 v[118:119], v[118:119], v[178:179]
	v_lshlrev_b32_e32 v170, 16, v171
	v_and_b32_e32 v171, 0xffff0000, v171
	v_pk_mul_f32 v[176:177], v[176:177], v[180:181]
	v_pk_mul_f32 v[118:119], v[118:119], v[182:183]
	v_pk_mul_f32 v[176:177], v[176:177], v[170:171]
	v_cvt_pk_bf16_f32 v124, v124, v125
	v_cvt_pk_bf16_f32 v125, v126, v127
	v_cvt_pk_bf16_f32 v126, v172, v173
	v_cvt_pk_bf16_f32 v127, v114, v115
	v_cvt_pk_bf16_f32 v168, v168, v169
	v_cvt_pk_bf16_f32 v169, v174, v175
	v_cvt_pk_bf16_f32 v170, v118, v119
	v_or_b32_e32 v118, 16, v152
	v_ashrrev_i32_e32 v119, 31, v118
	v_lshlrev_b64 v[114:115], 11, v[118:119]
	v_lshl_add_u64 v[114:115], s[6:7], 0, v[114:115]
	v_cvt_pk_bf16_f32 v171, v176, v177
	v_lshl_add_u64 v[114:115], v[114:115], 0, v[154:155]
	v_mov_b64_e32 v[172:173], v[196:197]
	v_mov_b64_e32 v[174:175], v[198:199]
	v_fmamk_f32 v104, v104, 0xbfb8aa3b, v150
	v_fmamk_f32 v105, v105, 0xbfb8aa3b, v151
	v_exp_f32_e32 v104, v104
	v_exp_f32_e32 v105, v105
	v_fmamk_f32 v106, v106, 0xbfb8aa3b, v148
	v_fmamk_f32 v107, v107, 0xbfb8aa3b, v149
	v_exp_f32_e32 v106, v106
	v_exp_f32_e32 v107, v107
	v_pk_add_f32 v[104:105], v[104:105], 1.0 op_sel_hi:[1,0]
	v_lshlrev_b64 v[114:115], 10, v[152:153]
	v_rcp_f32_e32 v104, v104
	v_pk_add_f32 v[106:107], v[106:107], 1.0 op_sel_hi:[1,0]
	v_rcp_f32_e32 v105, v105
	v_lshl_add_u64 v[114:115], v[114:115], 0, v[160:161]
	v_rcp_f32_e32 v106, v106
	v_rcp_f32_e32 v107, v107
	v_lshlrev_b64 v[114:115], 1, v[114:115]
	v_lshl_add_u64 v[176:177], s[40:41], 0, v[114:115]
	global_store_dwordx4 v[176:177], v[124:127], off
	v_pk_mul_f32 v[104:105], v[120:121], v[104:105]
	v_pk_mul_f32 v[106:107], v[122:123], v[106:107]
	v_lshl_add_u64 v[124:125], s[42:43], 0, v[114:115]
	global_store_dwordx4 v[124:125], v[168:171], off
	v_mul_f32_e32 v124, 0x4038aa3b, v104
	v_mul_f32_e32 v125, 0x4038aa3b, v105
	v_fmamk_f32 v108, v108, 0xbfb8aa3b, v158
	v_fmamk_f32 v109, v109, 0xbfb8aa3b, v159
	v_mul_f32_e32 v126, 0x4038aa3b, v106
	v_mul_f32_e32 v127, 0x4038aa3b, v107
	v_exp_f32_e32 v125, v125
	v_exp_f32_e32 v124, v124
	v_fmamk_f32 v96, v96, 0xbfb8aa3b, v142
	v_fmamk_f32 v97, v97, 0xbfb8aa3b, v143
	v_fmamk_f32 v98, v98, 0xbfb8aa3b, v140
	v_fmamk_f32 v99, v99, 0xbfb8aa3b, v141
	v_exp_f32_e32 v108, v108
	v_fmamk_f32 v110, v110, 0xbfb8aa3b, v156
	v_fmamk_f32 v111, v111, 0xbfb8aa3b, v157
	v_exp_f32_e32 v109, v109
	v_exp_f32_e32 v127, v127
	v_exp_f32_e32 v126, v126
	v_exp_f32_e32 v96, v96
	v_exp_f32_e32 v97, v97
	v_exp_f32_e32 v98, v98
	v_exp_f32_e32 v99, v99
	v_exp_f32_e32 v110, v110
	v_exp_f32_e32 v111, v111
	v_sub_f32_e32 v125, 1.0, v125
	v_sub_f32_e32 v124, 1.0, v124
	v_pk_add_f32 v[108:109], v[108:109], 1.0 op_sel_hi:[1,0]
	v_sub_f32_e32 v127, 1.0, v127
	v_sub_f32_e32 v126, 1.0, v126
	v_max_f32_e32 v124, 0, v124
	v_max_f32_e32 v125, 0, v125
	v_pk_add_f32 v[98:99], v[98:99], 1.0 op_sel_hi:[1,0]
	v_pk_add_f32 v[96:97], v[96:97], 1.0 op_sel_hi:[1,0]
	v_pk_add_f32 v[110:111], v[110:111], 1.0 op_sel_hi:[1,0]
	v_rcp_f32_e32 v108, v108
	v_rcp_f32_e32 v109, v109
	v_sqrt_f32_e32 v124, v124
	v_sqrt_f32_e32 v125, v125
	v_max_f32_e32 v126, 0, v126
	v_max_f32_e32 v127, 0, v127
	v_rcp_f32_e32 v96, v96
	v_rcp_f32_e32 v97, v97
	v_rcp_f32_e32 v98, v98
	v_rcp_f32_e32 v99, v99
	v_rcp_f32_e32 v110, v110
	v_rcp_f32_e32 v111, v111
	v_sqrt_f32_e32 v126, v126
	v_sqrt_f32_e32 v127, v127
	v_pk_mul_f32 v[108:109], v[108:109], v[124:125]
	v_pk_mul_f32 v[124:125], v[112:113], v[98:99]
	v_pk_mul_f32 v[98:99], v[116:117], v[96:97]
	v_pk_mul_f32 v[110:111], v[110:111], v[126:127]
	v_mul_f32_e32 v96, 0x4038aa3b, v98
	v_mul_f32_e32 v97, 0x4038aa3b, v99
	v_mul_f32_e32 v126, 0x4038aa3b, v124
	v_mul_f32_e32 v127, 0x4038aa3b, v125
	v_fmamk_f32 v100, v100, 0xbfb8aa3b, v146
	v_fmamk_f32 v101, v101, 0xbfb8aa3b, v147
	v_fmamk_f32 v102, v102, 0xbfb8aa3b, v144
	v_fmamk_f32 v103, v103, 0xbfb8aa3b, v145
	v_exp_f32_e32 v127, v127
	v_exp_f32_e32 v126, v126
	v_exp_f32_e32 v97, v97
	v_exp_f32_e32 v96, v96
	v_exp_f32_e32 v100, v100
	v_exp_f32_e32 v102, v102
	v_exp_f32_e32 v103, v103
	v_exp_f32_e32 v101, v101
	v_sub_f32_e32 v127, 1.0, v127
	v_sub_f32_e32 v126, 1.0, v126
	v_sub_f32_e32 v97, 1.0, v97
	v_sub_f32_e32 v96, 1.0, v96
	v_pk_add_f32 v[102:103], v[102:103], 1.0 op_sel_hi:[1,0]
	v_pk_add_f32 v[100:101], v[100:101], 1.0 op_sel_hi:[1,0]
	v_max_f32_e32 v96, 0, v96
	v_max_f32_e32 v97, 0, v97
	v_max_f32_e32 v126, 0, v126
	v_max_f32_e32 v127, 0, v127
	v_rcp_f32_e32 v100, v100
	v_rcp_f32_e32 v101, v101
	v_rcp_f32_e32 v102, v102
	v_rcp_f32_e32 v103, v103
	v_sqrt_f32_e32 v96, v96
	v_sqrt_f32_e32 v97, v97
	v_sqrt_f32_e32 v126, v126
	v_sqrt_f32_e32 v127, v127
	s_waitcnt vmcnt(2)
	v_lshlrev_b32_e32 v168, 16, v172
	v_and_b32_e32 v169, 0xffff0000, v172
	v_lshlrev_b32_e32 v170, 16, v173
	v_and_b32_e32 v171, 0xffff0000, v173
	v_pk_mul_f32 v[110:111], v[110:111], v[170:171]
	v_pk_mul_f32 v[108:109], v[108:109], v[168:169]
	v_lshlrev_b32_e32 v168, 16, v174
	v_and_b32_e32 v169, 0xffff0000, v174
	v_lshlrev_b32_e32 v170, 16, v175
	v_and_b32_e32 v171, 0xffff0000, v175
	v_pk_mul_f32 v[102:103], v[102:103], v[126:127]
	v_pk_mul_f32 v[96:97], v[100:101], v[96:97]
	v_pk_mul_f32 v[126:127], v[102:103], v[170:171]
	v_pk_mul_f32 v[102:103], v[96:97], v[168:169]
	v_cvt_pk_bf16_f32 v96, v104, v105
	v_cvt_pk_bf16_f32 v97, v106, v107
	v_cvt_pk_bf16_f32 v98, v98, v99
	v_cvt_pk_bf16_f32 v99, v124, v125
	v_cvt_pk_bf16_f32 v100, v108, v109
	v_or_b32_e32 v108, 32, v152
	v_ashrrev_i32_e32 v109, 31, v108
	v_lshlrev_b64 v[104:105], 11, v[108:109]
	v_lshl_add_u64 v[104:105], s[6:7], 0, v[104:105]
	v_cvt_pk_bf16_f32 v101, v110, v111
	v_cvt_pk_bf16_f32 v102, v102, v103
	v_cvt_pk_bf16_f32 v103, v126, v127
	v_lshl_add_u64 v[104:105], v[104:105], 0, v[154:155]
	v_mov_b64_e32 v[104:105], v[200:201]
	v_mov_b64_e32 v[106:107], v[202:203]
	v_fmamk_f32 v88, v88, 0xbfb8aa3b, v150
	v_fmamk_f32 v89, v89, 0xbfb8aa3b, v151
	v_exp_f32_e32 v88, v88
	v_exp_f32_e32 v89, v89
	v_fmamk_f32 v90, v90, 0xbfb8aa3b, v148
	v_fmamk_f32 v91, v91, 0xbfb8aa3b, v149
	v_exp_f32_e32 v90, v90
	v_exp_f32_e32 v91, v91
	v_pk_add_f32 v[88:89], v[88:89], 1.0 op_sel_hi:[1,0]
	v_lshlrev_b64 v[110:111], 10, v[118:119]
	v_rcp_f32_e32 v88, v88
	v_pk_add_f32 v[90:91], v[90:91], 1.0 op_sel_hi:[1,0]
	v_rcp_f32_e32 v89, v89
	v_lshl_add_u64 v[110:111], v[110:111], 0, v[160:161]
	v_rcp_f32_e32 v90, v90
	v_rcp_f32_e32 v91, v91
	v_lshlrev_b64 v[110:111], 1, v[110:111]
	v_lshl_add_u64 v[118:119], s[40:41], 0, v[110:111]
	global_store_dwordx4 v[118:119], v[96:99], off
	v_pk_mul_f32 v[88:89], v[120:121], v[88:89]
	v_pk_mul_f32 v[90:91], v[122:123], v[90:91]
	v_lshl_add_u64 v[96:97], s[42:43], 0, v[110:111]
	global_store_dwordx4 v[96:97], v[100:103], off
	v_mul_f32_e32 v96, 0x4038aa3b, v88
	v_mul_f32_e32 v97, 0x4038aa3b, v89
	v_fmamk_f32 v92, v92, 0xbfb8aa3b, v158
	v_fmamk_f32 v93, v93, 0xbfb8aa3b, v159
	v_mul_f32_e32 v98, 0x4038aa3b, v90
	v_mul_f32_e32 v99, 0x4038aa3b, v91
	v_exp_f32_e32 v97, v97
	v_exp_f32_e32 v96, v96
	v_fmamk_f32 v80, v80, 0xbfb8aa3b, v142
	v_fmamk_f32 v81, v81, 0xbfb8aa3b, v143
	v_fmamk_f32 v82, v82, 0xbfb8aa3b, v140
	v_fmamk_f32 v83, v83, 0xbfb8aa3b, v141
	v_exp_f32_e32 v92, v92
	v_fmamk_f32 v94, v94, 0xbfb8aa3b, v156
	v_fmamk_f32 v95, v95, 0xbfb8aa3b, v157
	v_exp_f32_e32 v93, v93
	v_exp_f32_e32 v99, v99
	v_exp_f32_e32 v98, v98
	v_exp_f32_e32 v80, v80
	v_exp_f32_e32 v81, v81
	v_exp_f32_e32 v82, v82
	v_exp_f32_e32 v83, v83
	v_exp_f32_e32 v94, v94
	v_exp_f32_e32 v95, v95
	v_sub_f32_e32 v97, 1.0, v97
	v_sub_f32_e32 v96, 1.0, v96
	v_pk_add_f32 v[92:93], v[92:93], 1.0 op_sel_hi:[1,0]
	v_sub_f32_e32 v99, 1.0, v99
	v_sub_f32_e32 v98, 1.0, v98
	v_max_f32_e32 v96, 0, v96
	v_max_f32_e32 v97, 0, v97
	v_pk_add_f32 v[82:83], v[82:83], 1.0 op_sel_hi:[1,0]
	v_pk_add_f32 v[80:81], v[80:81], 1.0 op_sel_hi:[1,0]
	v_pk_add_f32 v[94:95], v[94:95], 1.0 op_sel_hi:[1,0]
	v_rcp_f32_e32 v92, v92
	v_rcp_f32_e32 v93, v93
	v_sqrt_f32_e32 v96, v96
	v_sqrt_f32_e32 v97, v97
	v_max_f32_e32 v98, 0, v98
	v_max_f32_e32 v99, 0, v99
	v_rcp_f32_e32 v80, v80
	v_rcp_f32_e32 v81, v81
	v_rcp_f32_e32 v82, v82
	v_rcp_f32_e32 v83, v83
	v_rcp_f32_e32 v94, v94
	v_rcp_f32_e32 v95, v95
	v_sqrt_f32_e32 v98, v98
	v_sqrt_f32_e32 v99, v99
	v_pk_mul_f32 v[92:93], v[92:93], v[96:97]
	v_pk_mul_f32 v[96:97], v[112:113], v[82:83]
	v_pk_mul_f32 v[82:83], v[116:117], v[80:81]
	v_pk_mul_f32 v[94:95], v[94:95], v[98:99]
	v_mul_f32_e32 v80, 0x4038aa3b, v82
	v_mul_f32_e32 v81, 0x4038aa3b, v83
	v_mul_f32_e32 v98, 0x4038aa3b, v96
	v_mul_f32_e32 v99, 0x4038aa3b, v97
	v_fmamk_f32 v84, v84, 0xbfb8aa3b, v146
	v_fmamk_f32 v85, v85, 0xbfb8aa3b, v147
	v_fmamk_f32 v86, v86, 0xbfb8aa3b, v144
	v_fmamk_f32 v87, v87, 0xbfb8aa3b, v145
	v_exp_f32_e32 v99, v99
	v_exp_f32_e32 v98, v98
	v_exp_f32_e32 v81, v81
	v_exp_f32_e32 v80, v80
	v_exp_f32_e32 v84, v84
	v_exp_f32_e32 v86, v86
	v_exp_f32_e32 v87, v87
	v_exp_f32_e32 v85, v85
	v_sub_f32_e32 v99, 1.0, v99
	v_sub_f32_e32 v98, 1.0, v98
	v_sub_f32_e32 v81, 1.0, v81
	v_sub_f32_e32 v80, 1.0, v80
	v_pk_add_f32 v[86:87], v[86:87], 1.0 op_sel_hi:[1,0]
	v_pk_add_f32 v[84:85], v[84:85], 1.0 op_sel_hi:[1,0]
	v_max_f32_e32 v80, 0, v80
	v_max_f32_e32 v81, 0, v81
	v_max_f32_e32 v98, 0, v98
	v_max_f32_e32 v99, 0, v99
	v_rcp_f32_e32 v84, v84
	v_rcp_f32_e32 v85, v85
	v_rcp_f32_e32 v86, v86
	v_rcp_f32_e32 v87, v87
	v_sqrt_f32_e32 v80, v80
	v_sqrt_f32_e32 v81, v81
	v_sqrt_f32_e32 v98, v98
	v_sqrt_f32_e32 v99, v99
	s_waitcnt vmcnt(2)
	v_lshlrev_b32_e32 v100, 16, v104
	v_and_b32_e32 v101, 0xffff0000, v104
	v_lshlrev_b32_e32 v102, 16, v105
	v_and_b32_e32 v103, 0xffff0000, v105
	v_pk_mul_f32 v[94:95], v[94:95], v[102:103]
	v_pk_mul_f32 v[92:93], v[92:93], v[100:101]
	v_lshlrev_b32_e32 v100, 16, v106
	v_and_b32_e32 v101, 0xffff0000, v106
	v_lshlrev_b32_e32 v102, 16, v107
	v_and_b32_e32 v103, 0xffff0000, v107
	v_pk_mul_f32 v[86:87], v[86:87], v[98:99]
	v_pk_mul_f32 v[80:81], v[84:85], v[80:81]
	v_pk_mul_f32 v[98:99], v[86:87], v[102:103]
	v_pk_mul_f32 v[86:87], v[80:81], v[100:101]
	v_cvt_pk_bf16_f32 v80, v88, v89
	v_cvt_pk_bf16_f32 v81, v90, v91
	v_cvt_pk_bf16_f32 v82, v82, v83
	v_cvt_pk_bf16_f32 v83, v96, v97
	v_cvt_pk_bf16_f32 v84, v92, v93
	v_or_b32_e32 v92, 48, v152
	v_ashrrev_i32_e32 v93, 31, v92
	v_lshlrev_b64 v[88:89], 11, v[92:93]
	v_lshl_add_u64 v[88:89], s[6:7], 0, v[88:89]
	v_cvt_pk_bf16_f32 v85, v94, v95
	v_cvt_pk_bf16_f32 v86, v86, v87
	v_cvt_pk_bf16_f32 v87, v98, v99
	v_lshl_add_u64 v[88:89], v[88:89], 0, v[154:155]
	v_mov_b64_e32 v[88:89], v[204:205]
	v_mov_b64_e32 v[90:91], v[206:207]
	v_fmamk_f32 v72, v72, 0xbfb8aa3b, v150
	v_fmamk_f32 v73, v73, 0xbfb8aa3b, v151
	v_exp_f32_e32 v72, v72
	v_exp_f32_e32 v73, v73
	v_fmamk_f32 v74, v74, 0xbfb8aa3b, v148
	v_fmamk_f32 v75, v75, 0xbfb8aa3b, v149
	v_exp_f32_e32 v74, v74
	v_exp_f32_e32 v75, v75
	v_pk_add_f32 v[72:73], v[72:73], 1.0 op_sel_hi:[1,0]
	v_lshlrev_b64 v[94:95], 10, v[108:109]
	v_rcp_f32_e32 v72, v72
	v_pk_add_f32 v[74:75], v[74:75], 1.0 op_sel_hi:[1,0]
	v_rcp_f32_e32 v73, v73
	v_lshl_add_u64 v[94:95], v[94:95], 0, v[160:161]
	v_rcp_f32_e32 v74, v74
	v_rcp_f32_e32 v75, v75
	v_lshlrev_b64 v[94:95], 1, v[94:95]
	v_lshl_add_u64 v[96:97], s[40:41], 0, v[94:95]
	global_store_dwordx4 v[96:97], v[80:83], off
	v_pk_mul_f32 v[72:73], v[120:121], v[72:73]
	v_pk_mul_f32 v[74:75], v[122:123], v[74:75]
	v_lshl_add_u64 v[80:81], s[42:43], 0, v[94:95]
	global_store_dwordx4 v[80:81], v[84:87], off
	v_mul_f32_e32 v80, 0x4038aa3b, v72
	v_mul_f32_e32 v81, 0x4038aa3b, v73
	v_fmamk_f32 v76, v76, 0xbfb8aa3b, v158
	v_fmamk_f32 v77, v77, 0xbfb8aa3b, v159
	v_mul_f32_e32 v82, 0x4038aa3b, v74
	v_mul_f32_e32 v83, 0x4038aa3b, v75
	v_exp_f32_e32 v81, v81
	v_exp_f32_e32 v80, v80
	v_fmamk_f32 v64, v64, 0xbfb8aa3b, v142
	v_fmamk_f32 v65, v65, 0xbfb8aa3b, v143
	v_fmamk_f32 v66, v66, 0xbfb8aa3b, v140
	v_fmamk_f32 v67, v67, 0xbfb8aa3b, v141
	v_exp_f32_e32 v76, v76
	v_fmamk_f32 v78, v78, 0xbfb8aa3b, v156
	v_fmamk_f32 v79, v79, 0xbfb8aa3b, v157
	v_exp_f32_e32 v77, v77
	v_exp_f32_e32 v83, v83
	v_exp_f32_e32 v82, v82
	v_exp_f32_e32 v64, v64
	v_exp_f32_e32 v65, v65
	v_exp_f32_e32 v66, v66
	v_exp_f32_e32 v67, v67
	v_exp_f32_e32 v78, v78
	v_exp_f32_e32 v79, v79
	v_sub_f32_e32 v81, 1.0, v81
	v_sub_f32_e32 v80, 1.0, v80
	v_pk_add_f32 v[76:77], v[76:77], 1.0 op_sel_hi:[1,0]
	v_sub_f32_e32 v83, 1.0, v83
	v_sub_f32_e32 v82, 1.0, v82
	v_max_f32_e32 v80, 0, v80
	v_max_f32_e32 v81, 0, v81
	v_pk_add_f32 v[66:67], v[66:67], 1.0 op_sel_hi:[1,0]
	v_pk_add_f32 v[64:65], v[64:65], 1.0 op_sel_hi:[1,0]
	v_pk_add_f32 v[78:79], v[78:79], 1.0 op_sel_hi:[1,0]
	v_rcp_f32_e32 v76, v76
	v_rcp_f32_e32 v77, v77
	v_sqrt_f32_e32 v80, v80
	v_sqrt_f32_e32 v81, v81
	v_max_f32_e32 v82, 0, v82
	v_max_f32_e32 v83, 0, v83
	v_rcp_f32_e32 v64, v64
	v_rcp_f32_e32 v65, v65
	v_rcp_f32_e32 v66, v66
	v_rcp_f32_e32 v67, v67
	v_rcp_f32_e32 v78, v78
	v_rcp_f32_e32 v79, v79
	v_sqrt_f32_e32 v82, v82
	v_sqrt_f32_e32 v83, v83
	v_pk_mul_f32 v[76:77], v[76:77], v[80:81]
	v_pk_mul_f32 v[80:81], v[112:113], v[66:67]
	v_pk_mul_f32 v[66:67], v[116:117], v[64:65]
	v_pk_mul_f32 v[78:79], v[78:79], v[82:83]
	v_mul_f32_e32 v64, 0x4038aa3b, v66
	v_mul_f32_e32 v65, 0x4038aa3b, v67
	v_mul_f32_e32 v82, 0x4038aa3b, v80
	v_mul_f32_e32 v83, 0x4038aa3b, v81
	v_fmamk_f32 v68, v68, 0xbfb8aa3b, v146
	v_fmamk_f32 v69, v69, 0xbfb8aa3b, v147
	v_fmamk_f32 v70, v70, 0xbfb8aa3b, v144
	v_fmamk_f32 v71, v71, 0xbfb8aa3b, v145
	v_exp_f32_e32 v83, v83
	v_exp_f32_e32 v82, v82
	v_exp_f32_e32 v65, v65
	v_exp_f32_e32 v64, v64
	v_exp_f32_e32 v68, v68
	v_exp_f32_e32 v70, v70
	v_exp_f32_e32 v71, v71
	v_exp_f32_e32 v69, v69
	v_sub_f32_e32 v83, 1.0, v83
	v_sub_f32_e32 v82, 1.0, v82
	v_sub_f32_e32 v65, 1.0, v65
	v_sub_f32_e32 v64, 1.0, v64
	v_pk_add_f32 v[70:71], v[70:71], 1.0 op_sel_hi:[1,0]
	v_pk_add_f32 v[68:69], v[68:69], 1.0 op_sel_hi:[1,0]
	v_max_f32_e32 v64, 0, v64
	v_max_f32_e32 v65, 0, v65
	v_max_f32_e32 v82, 0, v82
	v_max_f32_e32 v83, 0, v83
	v_rcp_f32_e32 v68, v68
	v_rcp_f32_e32 v69, v69
	v_rcp_f32_e32 v70, v70
	v_rcp_f32_e32 v71, v71
	v_sqrt_f32_e32 v64, v64
	v_sqrt_f32_e32 v65, v65
	v_sqrt_f32_e32 v82, v82
	v_sqrt_f32_e32 v83, v83
	s_waitcnt vmcnt(2)
	v_lshlrev_b32_e32 v84, 16, v88
	v_and_b32_e32 v85, 0xffff0000, v88
	v_lshlrev_b32_e32 v86, 16, v89
	v_and_b32_e32 v87, 0xffff0000, v89
	v_pk_mul_f32 v[78:79], v[78:79], v[86:87]
	v_pk_mul_f32 v[76:77], v[76:77], v[84:85]
	v_lshlrev_b32_e32 v84, 16, v90
	v_and_b32_e32 v85, 0xffff0000, v90
	v_lshlrev_b32_e32 v86, 16, v91
	v_and_b32_e32 v87, 0xffff0000, v91
	v_pk_mul_f32 v[70:71], v[70:71], v[82:83]
	v_pk_mul_f32 v[64:65], v[68:69], v[64:65]
	v_pk_mul_f32 v[82:83], v[70:71], v[86:87]
	v_pk_mul_f32 v[70:71], v[64:65], v[84:85]
	v_cvt_pk_bf16_f32 v64, v72, v73
	v_cvt_pk_bf16_f32 v65, v74, v75
	v_cvt_pk_bf16_f32 v66, v66, v67
	v_cvt_pk_bf16_f32 v67, v80, v81
	v_cvt_pk_bf16_f32 v68, v76, v77
	v_add_u32_e32 v76, 0x80, v152
	v_ashrrev_i32_e32 v77, 31, v76
	v_lshlrev_b64 v[72:73], 11, v[76:77]
	v_lshl_add_u64 v[72:73], s[6:7], 0, v[72:73]
	v_cvt_pk_bf16_f32 v69, v78, v79
	v_cvt_pk_bf16_f32 v70, v70, v71
	v_cvt_pk_bf16_f32 v71, v82, v83
	v_lshl_add_u64 v[72:73], v[72:73], 0, v[154:155]
	v_mov_b64_e32 v[72:73], v[208:209]
	v_mov_b64_e32 v[74:75], v[210:211]
	v_fmamk_f32 v56, v56, 0xbfb8aa3b, v150
	v_fmamk_f32 v57, v57, 0xbfb8aa3b, v151
	v_exp_f32_e32 v56, v56
	v_exp_f32_e32 v57, v57
	v_fmamk_f32 v58, v58, 0xbfb8aa3b, v148
	v_fmamk_f32 v59, v59, 0xbfb8aa3b, v149
	v_exp_f32_e32 v58, v58
	v_exp_f32_e32 v59, v59
	v_pk_add_f32 v[56:57], v[56:57], 1.0 op_sel_hi:[1,0]
	v_lshlrev_b64 v[78:79], 10, v[92:93]
	v_rcp_f32_e32 v56, v56
	v_pk_add_f32 v[58:59], v[58:59], 1.0 op_sel_hi:[1,0]
	v_rcp_f32_e32 v57, v57
	v_lshl_add_u64 v[78:79], v[78:79], 0, v[160:161]
	v_rcp_f32_e32 v58, v58
	v_rcp_f32_e32 v59, v59
	v_lshlrev_b64 v[78:79], 1, v[78:79]
	v_lshl_add_u64 v[80:81], s[40:41], 0, v[78:79]
	global_store_dwordx4 v[80:81], v[64:67], off
	v_pk_mul_f32 v[56:57], v[120:121], v[56:57]
	v_pk_mul_f32 v[58:59], v[122:123], v[58:59]
	v_lshl_add_u64 v[64:65], s[42:43], 0, v[78:79]
	global_store_dwordx4 v[64:65], v[68:71], off
	v_mul_f32_e32 v64, 0x4038aa3b, v56
	v_mul_f32_e32 v65, 0x4038aa3b, v57
	v_fmamk_f32 v60, v60, 0xbfb8aa3b, v158
	v_fmamk_f32 v61, v61, 0xbfb8aa3b, v159
	v_mul_f32_e32 v66, 0x4038aa3b, v58
	v_mul_f32_e32 v67, 0x4038aa3b, v59
	v_exp_f32_e32 v65, v65
	v_exp_f32_e32 v64, v64
	v_fmamk_f32 v48, v48, 0xbfb8aa3b, v142
	v_fmamk_f32 v49, v49, 0xbfb8aa3b, v143
	v_fmamk_f32 v50, v50, 0xbfb8aa3b, v140
	v_fmamk_f32 v51, v51, 0xbfb8aa3b, v141
	v_exp_f32_e32 v60, v60
	v_fmamk_f32 v62, v62, 0xbfb8aa3b, v156
	v_fmamk_f32 v63, v63, 0xbfb8aa3b, v157
	v_exp_f32_e32 v61, v61
	v_exp_f32_e32 v67, v67
	v_exp_f32_e32 v66, v66
	v_exp_f32_e32 v48, v48
	v_exp_f32_e32 v49, v49
	v_exp_f32_e32 v50, v50
	v_exp_f32_e32 v51, v51
	v_exp_f32_e32 v62, v62
	v_exp_f32_e32 v63, v63
	v_sub_f32_e32 v65, 1.0, v65
	v_sub_f32_e32 v64, 1.0, v64
	v_pk_add_f32 v[60:61], v[60:61], 1.0 op_sel_hi:[1,0]
	v_sub_f32_e32 v67, 1.0, v67
	v_sub_f32_e32 v66, 1.0, v66
	v_max_f32_e32 v64, 0, v64
	v_max_f32_e32 v65, 0, v65
	v_pk_add_f32 v[50:51], v[50:51], 1.0 op_sel_hi:[1,0]
	v_pk_add_f32 v[48:49], v[48:49], 1.0 op_sel_hi:[1,0]
	v_pk_add_f32 v[62:63], v[62:63], 1.0 op_sel_hi:[1,0]
	v_rcp_f32_e32 v60, v60
	v_rcp_f32_e32 v61, v61
	v_sqrt_f32_e32 v64, v64
	v_sqrt_f32_e32 v65, v65
	v_max_f32_e32 v66, 0, v66
	v_max_f32_e32 v67, 0, v67
	v_rcp_f32_e32 v48, v48
	v_rcp_f32_e32 v49, v49
	v_rcp_f32_e32 v50, v50
	v_rcp_f32_e32 v51, v51
	v_rcp_f32_e32 v62, v62
	v_rcp_f32_e32 v63, v63
	v_sqrt_f32_e32 v66, v66
	v_sqrt_f32_e32 v67, v67
	v_pk_mul_f32 v[60:61], v[60:61], v[64:65]
	v_pk_mul_f32 v[64:65], v[112:113], v[50:51]
	v_pk_mul_f32 v[50:51], v[116:117], v[48:49]
	v_pk_mul_f32 v[62:63], v[62:63], v[66:67]
	v_mul_f32_e32 v48, 0x4038aa3b, v50
	v_mul_f32_e32 v49, 0x4038aa3b, v51
	v_mul_f32_e32 v66, 0x4038aa3b, v64
	v_mul_f32_e32 v67, 0x4038aa3b, v65
	v_fmamk_f32 v52, v52, 0xbfb8aa3b, v146
	v_fmamk_f32 v53, v53, 0xbfb8aa3b, v147
	v_fmamk_f32 v54, v54, 0xbfb8aa3b, v144
	v_fmamk_f32 v55, v55, 0xbfb8aa3b, v145
	v_exp_f32_e32 v67, v67
	v_exp_f32_e32 v66, v66
	v_exp_f32_e32 v49, v49
	v_exp_f32_e32 v48, v48
	v_exp_f32_e32 v52, v52
	v_exp_f32_e32 v54, v54
	v_exp_f32_e32 v55, v55
	v_exp_f32_e32 v53, v53
	v_sub_f32_e32 v67, 1.0, v67
	v_sub_f32_e32 v66, 1.0, v66
	v_sub_f32_e32 v49, 1.0, v49
	v_sub_f32_e32 v48, 1.0, v48
	v_pk_add_f32 v[54:55], v[54:55], 1.0 op_sel_hi:[1,0]
	v_pk_add_f32 v[52:53], v[52:53], 1.0 op_sel_hi:[1,0]
	v_max_f32_e32 v48, 0, v48
	v_max_f32_e32 v49, 0, v49
	v_max_f32_e32 v66, 0, v66
	v_max_f32_e32 v67, 0, v67
	v_rcp_f32_e32 v52, v52
	v_rcp_f32_e32 v53, v53
	v_rcp_f32_e32 v54, v54
	v_rcp_f32_e32 v55, v55
	v_sqrt_f32_e32 v48, v48
	v_sqrt_f32_e32 v49, v49
	v_sqrt_f32_e32 v66, v66
	v_sqrt_f32_e32 v67, v67
	s_waitcnt vmcnt(2)
	v_lshlrev_b32_e32 v68, 16, v72
	v_and_b32_e32 v69, 0xffff0000, v72
	v_lshlrev_b32_e32 v70, 16, v73
	v_and_b32_e32 v71, 0xffff0000, v73
	v_pk_mul_f32 v[62:63], v[62:63], v[70:71]
	v_pk_mul_f32 v[60:61], v[60:61], v[68:69]
	v_lshlrev_b32_e32 v68, 16, v74
	v_and_b32_e32 v69, 0xffff0000, v74
	v_lshlrev_b32_e32 v70, 16, v75
	v_and_b32_e32 v71, 0xffff0000, v75
	v_pk_mul_f32 v[54:55], v[54:55], v[66:67]
	v_pk_mul_f32 v[48:49], v[52:53], v[48:49]
	v_pk_mul_f32 v[66:67], v[54:55], v[70:71]
	v_pk_mul_f32 v[54:55], v[48:49], v[68:69]
	v_cvt_pk_bf16_f32 v48, v56, v57
	v_add_u32_e32 v56, 0x90, v152
	v_ashrrev_i32_e32 v57, 31, v56
	v_lshlrev_b64 v[56:57], 11, v[56:57]
	v_lshl_add_u64 v[56:57], s[6:7], 0, v[56:57]
	v_cvt_pk_bf16_f32 v49, v58, v59
	v_cvt_pk_bf16_f32 v50, v50, v51
	v_cvt_pk_bf16_f32 v51, v64, v65
	v_cvt_pk_bf16_f32 v52, v60, v61
	v_cvt_pk_bf16_f32 v53, v62, v63
	v_cvt_pk_bf16_f32 v54, v54, v55
	v_cvt_pk_bf16_f32 v55, v66, v67
	v_lshl_add_u64 v[56:57], v[56:57], 0, v[154:155]
	v_mov_b64_e32 v[56:57], v[212:213]
	v_mov_b64_e32 v[58:59], v[214:215]
	v_fmamk_f32 v40, v40, 0xbfb8aa3b, v150
	v_fmamk_f32 v41, v41, 0xbfb8aa3b, v151
	v_exp_f32_e32 v40, v40
	v_exp_f32_e32 v41, v41
	v_fmamk_f32 v42, v42, 0xbfb8aa3b, v148
	v_fmamk_f32 v43, v43, 0xbfb8aa3b, v149
	v_exp_f32_e32 v42, v42
	v_exp_f32_e32 v43, v43
	v_pk_add_f32 v[40:41], v[40:41], 1.0 op_sel_hi:[1,0]
	v_lshlrev_b64 v[60:61], 10, v[76:77]
	v_rcp_f32_e32 v40, v40
	v_pk_add_f32 v[42:43], v[42:43], 1.0 op_sel_hi:[1,0]
	v_rcp_f32_e32 v41, v41
	v_lshl_add_u64 v[60:61], v[60:61], 0, v[160:161]
	v_rcp_f32_e32 v42, v42
	v_rcp_f32_e32 v43, v43
	v_lshlrev_b64 v[60:61], 1, v[60:61]
	v_lshl_add_u64 v[62:63], s[40:41], 0, v[60:61]
	global_store_dwordx4 v[62:63], v[48:51], off
	v_pk_mul_f32 v[40:41], v[120:121], v[40:41]
	v_pk_mul_f32 v[42:43], v[122:123], v[42:43]
	v_lshl_add_u64 v[48:49], s[42:43], 0, v[60:61]
	global_store_dwordx4 v[48:49], v[52:55], off
	v_mul_f32_e32 v48, 0x4038aa3b, v40
	v_mul_f32_e32 v49, 0x4038aa3b, v41
	v_fmamk_f32 v44, v44, 0xbfb8aa3b, v158
	v_fmamk_f32 v45, v45, 0xbfb8aa3b, v159
	v_mul_f32_e32 v50, 0x4038aa3b, v42
	v_mul_f32_e32 v51, 0x4038aa3b, v43
	v_exp_f32_e32 v49, v49
	v_exp_f32_e32 v48, v48
	v_fmamk_f32 v32, v32, 0xbfb8aa3b, v142
	v_fmamk_f32 v33, v33, 0xbfb8aa3b, v143
	v_fmamk_f32 v34, v34, 0xbfb8aa3b, v140
	v_fmamk_f32 v35, v35, 0xbfb8aa3b, v141
	v_exp_f32_e32 v44, v44
	v_fmamk_f32 v46, v46, 0xbfb8aa3b, v156
	v_fmamk_f32 v47, v47, 0xbfb8aa3b, v157
	v_exp_f32_e32 v45, v45
	v_exp_f32_e32 v51, v51
	v_exp_f32_e32 v50, v50
	v_exp_f32_e32 v32, v32
	v_exp_f32_e32 v33, v33
	v_exp_f32_e32 v34, v34
	v_exp_f32_e32 v35, v35
	v_exp_f32_e32 v46, v46
	v_exp_f32_e32 v47, v47
	v_sub_f32_e32 v49, 1.0, v49
	v_sub_f32_e32 v48, 1.0, v48
	v_pk_add_f32 v[44:45], v[44:45], 1.0 op_sel_hi:[1,0]
	v_sub_f32_e32 v51, 1.0, v51
	v_sub_f32_e32 v50, 1.0, v50
	v_max_f32_e32 v48, 0, v48
	v_max_f32_e32 v49, 0, v49
	v_pk_add_f32 v[34:35], v[34:35], 1.0 op_sel_hi:[1,0]
	v_pk_add_f32 v[32:33], v[32:33], 1.0 op_sel_hi:[1,0]
	v_pk_add_f32 v[46:47], v[46:47], 1.0 op_sel_hi:[1,0]
	v_rcp_f32_e32 v44, v44
	v_rcp_f32_e32 v45, v45
	v_sqrt_f32_e32 v48, v48
	v_sqrt_f32_e32 v49, v49
	v_max_f32_e32 v50, 0, v50
	v_max_f32_e32 v51, 0, v51
	v_rcp_f32_e32 v32, v32
	v_rcp_f32_e32 v33, v33
	v_rcp_f32_e32 v34, v34
	v_rcp_f32_e32 v35, v35
	v_rcp_f32_e32 v46, v46
	v_rcp_f32_e32 v47, v47
	v_sqrt_f32_e32 v50, v50
	v_sqrt_f32_e32 v51, v51
	v_pk_mul_f32 v[44:45], v[44:45], v[48:49]
	v_pk_mul_f32 v[48:49], v[112:113], v[34:35]
	v_pk_mul_f32 v[34:35], v[116:117], v[32:33]
	v_pk_mul_f32 v[46:47], v[46:47], v[50:51]
	v_mul_f32_e32 v32, 0x4038aa3b, v34
	v_mul_f32_e32 v33, 0x4038aa3b, v35
	v_mul_f32_e32 v50, 0x4038aa3b, v48
	v_mul_f32_e32 v51, 0x4038aa3b, v49
	v_fmamk_f32 v36, v36, 0xbfb8aa3b, v146
	v_fmamk_f32 v37, v37, 0xbfb8aa3b, v147
	v_fmamk_f32 v38, v38, 0xbfb8aa3b, v144
	v_fmamk_f32 v39, v39, 0xbfb8aa3b, v145
	v_exp_f32_e32 v51, v51
	v_exp_f32_e32 v50, v50
	v_exp_f32_e32 v33, v33
	v_exp_f32_e32 v32, v32
	v_exp_f32_e32 v36, v36
	v_exp_f32_e32 v38, v38
	v_exp_f32_e32 v39, v39
	v_exp_f32_e32 v37, v37
	v_sub_f32_e32 v51, 1.0, v51
	v_sub_f32_e32 v50, 1.0, v50
	v_sub_f32_e32 v33, 1.0, v33
	v_sub_f32_e32 v32, 1.0, v32
	v_pk_add_f32 v[38:39], v[38:39], 1.0 op_sel_hi:[1,0]
	v_pk_add_f32 v[36:37], v[36:37], 1.0 op_sel_hi:[1,0]
	v_max_f32_e32 v32, 0, v32
	v_max_f32_e32 v33, 0, v33
	v_max_f32_e32 v50, 0, v50
	v_max_f32_e32 v51, 0, v51
	v_rcp_f32_e32 v36, v36
	v_rcp_f32_e32 v37, v37
	v_rcp_f32_e32 v38, v38
	v_rcp_f32_e32 v39, v39
	v_sqrt_f32_e32 v32, v32
	v_sqrt_f32_e32 v33, v33
	v_sqrt_f32_e32 v50, v50
	v_sqrt_f32_e32 v51, v51
	s_waitcnt vmcnt(2)
	v_lshlrev_b32_e32 v52, 16, v56
	v_and_b32_e32 v53, 0xffff0000, v56
	v_lshlrev_b32_e32 v54, 16, v57
	v_and_b32_e32 v55, 0xffff0000, v57
	v_pk_mul_f32 v[46:47], v[46:47], v[54:55]
	v_pk_mul_f32 v[44:45], v[44:45], v[52:53]
	v_lshlrev_b32_e32 v52, 16, v58
	v_and_b32_e32 v53, 0xffff0000, v58
	v_lshlrev_b32_e32 v54, 16, v59
	v_and_b32_e32 v55, 0xffff0000, v59
	v_pk_mul_f32 v[38:39], v[38:39], v[50:51]
	v_pk_mul_f32 v[32:33], v[36:37], v[32:33]
	v_pk_mul_f32 v[50:51], v[38:39], v[54:55]
	v_pk_mul_f32 v[38:39], v[32:33], v[52:53]
	v_cvt_pk_bf16_f32 v32, v40, v41
	v_add_u32_e32 v40, 0xa0, v152
	v_ashrrev_i32_e32 v41, 31, v40
	v_lshlrev_b64 v[40:41], 11, v[40:41]
	v_lshl_add_u64 v[40:41], s[6:7], 0, v[40:41]
	v_cvt_pk_bf16_f32 v33, v42, v43
	v_cvt_pk_bf16_f32 v34, v34, v35
	v_cvt_pk_bf16_f32 v35, v48, v49
	v_cvt_pk_bf16_f32 v36, v44, v45
	v_cvt_pk_bf16_f32 v37, v46, v47
	v_cvt_pk_bf16_f32 v38, v38, v39
	v_cvt_pk_bf16_f32 v39, v50, v51
	v_lshl_add_u64 v[40:41], v[40:41], 0, v[154:155]
	v_mov_b64_e32 v[40:41], v[216:217]
	v_mov_b64_e32 v[42:43], v[218:219]
	v_fmamk_f32 v24, v24, 0xbfb8aa3b, v150
	v_fmamk_f32 v25, v25, 0xbfb8aa3b, v151
	v_exp_f32_e32 v24, v24
	v_exp_f32_e32 v25, v25
	v_fmamk_f32 v26, v26, 0xbfb8aa3b, v148
	v_fmamk_f32 v27, v27, 0xbfb8aa3b, v149
	v_exp_f32_e32 v26, v26
	v_exp_f32_e32 v27, v27
	v_pk_add_f32 v[24:25], v[24:25], 1.0 op_sel_hi:[1,0]
	v_lshl_add_u64 v[44:45], v[114:115], 0, s[24:25]
	v_rcp_f32_e32 v24, v24
	v_pk_add_f32 v[26:27], v[26:27], 1.0 op_sel_hi:[1,0]
	v_rcp_f32_e32 v25, v25
	v_rcp_f32_e32 v26, v26
	v_rcp_f32_e32 v27, v27
	v_lshl_add_u64 v[46:47], s[40:41], 0, v[44:45]
	global_store_dwordx4 v[46:47], v[32:35], off
	v_pk_mul_f32 v[24:25], v[120:121], v[24:25]
	v_pk_mul_f32 v[26:27], v[122:123], v[26:27]
	v_lshl_add_u64 v[32:33], s[42:43], 0, v[44:45]
	global_store_dwordx4 v[32:33], v[36:39], off
	v_mul_f32_e32 v32, 0x4038aa3b, v24
	v_mul_f32_e32 v33, 0x4038aa3b, v25
	v_fmamk_f32 v28, v28, 0xbfb8aa3b, v158
	v_fmamk_f32 v29, v29, 0xbfb8aa3b, v159
	v_mul_f32_e32 v34, 0x4038aa3b, v26
	v_mul_f32_e32 v35, 0x4038aa3b, v27
	v_exp_f32_e32 v33, v33
	v_exp_f32_e32 v32, v32
	v_fmamk_f32 v16, v16, 0xbfb8aa3b, v142
	v_fmamk_f32 v17, v17, 0xbfb8aa3b, v143
	v_fmamk_f32 v18, v18, 0xbfb8aa3b, v140
	v_fmamk_f32 v19, v19, 0xbfb8aa3b, v141
	v_exp_f32_e32 v28, v28
	v_fmamk_f32 v30, v30, 0xbfb8aa3b, v156
	v_fmamk_f32 v31, v31, 0xbfb8aa3b, v157
	v_exp_f32_e32 v29, v29
	v_exp_f32_e32 v35, v35
	v_exp_f32_e32 v34, v34
	v_exp_f32_e32 v16, v16
	v_exp_f32_e32 v17, v17
	v_exp_f32_e32 v18, v18
	v_exp_f32_e32 v19, v19
	v_exp_f32_e32 v30, v30
	v_exp_f32_e32 v31, v31
	v_sub_f32_e32 v33, 1.0, v33
	v_sub_f32_e32 v32, 1.0, v32
	v_pk_add_f32 v[28:29], v[28:29], 1.0 op_sel_hi:[1,0]
	v_sub_f32_e32 v35, 1.0, v35
	v_sub_f32_e32 v34, 1.0, v34
	v_max_f32_e32 v32, 0, v32
	v_max_f32_e32 v33, 0, v33
	v_pk_add_f32 v[18:19], v[18:19], 1.0 op_sel_hi:[1,0]
	v_pk_add_f32 v[16:17], v[16:17], 1.0 op_sel_hi:[1,0]
	v_pk_add_f32 v[30:31], v[30:31], 1.0 op_sel_hi:[1,0]
	v_rcp_f32_e32 v28, v28
	v_rcp_f32_e32 v29, v29
	v_sqrt_f32_e32 v32, v32
	v_sqrt_f32_e32 v33, v33
	v_max_f32_e32 v34, 0, v34
	v_max_f32_e32 v35, 0, v35
	v_rcp_f32_e32 v16, v16
	v_rcp_f32_e32 v17, v17
	v_rcp_f32_e32 v18, v18
	v_rcp_f32_e32 v19, v19
	v_rcp_f32_e32 v30, v30
	v_rcp_f32_e32 v31, v31
	v_sqrt_f32_e32 v34, v34
	v_sqrt_f32_e32 v35, v35
	v_pk_mul_f32 v[28:29], v[28:29], v[32:33]
	v_pk_mul_f32 v[32:33], v[112:113], v[18:19]
	v_pk_mul_f32 v[18:19], v[116:117], v[16:17]
	v_pk_mul_f32 v[30:31], v[30:31], v[34:35]
	v_mul_f32_e32 v16, 0x4038aa3b, v18
	v_mul_f32_e32 v17, 0x4038aa3b, v19
	v_mul_f32_e32 v34, 0x4038aa3b, v32
	v_mul_f32_e32 v35, 0x4038aa3b, v33
	v_fmamk_f32 v20, v20, 0xbfb8aa3b, v146
	v_fmamk_f32 v21, v21, 0xbfb8aa3b, v147
	v_fmamk_f32 v22, v22, 0xbfb8aa3b, v144
	v_fmamk_f32 v23, v23, 0xbfb8aa3b, v145
	v_exp_f32_e32 v35, v35
	v_exp_f32_e32 v34, v34
	v_exp_f32_e32 v17, v17
	v_exp_f32_e32 v16, v16
	v_exp_f32_e32 v20, v20
	v_exp_f32_e32 v22, v22
	v_exp_f32_e32 v23, v23
	v_exp_f32_e32 v21, v21
	v_sub_f32_e32 v35, 1.0, v35
	v_sub_f32_e32 v34, 1.0, v34
	v_sub_f32_e32 v17, 1.0, v17
	v_sub_f32_e32 v16, 1.0, v16
	v_pk_add_f32 v[22:23], v[22:23], 1.0 op_sel_hi:[1,0]
	v_pk_add_f32 v[20:21], v[20:21], 1.0 op_sel_hi:[1,0]
	v_max_f32_e32 v16, 0, v16
	v_max_f32_e32 v17, 0, v17
	v_max_f32_e32 v34, 0, v34
	v_max_f32_e32 v35, 0, v35
	v_rcp_f32_e32 v20, v20
	v_rcp_f32_e32 v21, v21
	v_rcp_f32_e32 v22, v22
	v_rcp_f32_e32 v23, v23
	v_sqrt_f32_e32 v16, v16
	v_sqrt_f32_e32 v17, v17
	v_sqrt_f32_e32 v34, v34
	v_sqrt_f32_e32 v35, v35
	s_waitcnt vmcnt(2)
	v_lshlrev_b32_e32 v36, 16, v40
	v_and_b32_e32 v37, 0xffff0000, v40
	v_lshlrev_b32_e32 v38, 16, v41
	v_and_b32_e32 v39, 0xffff0000, v41
	v_pk_mul_f32 v[30:31], v[30:31], v[38:39]
	v_pk_mul_f32 v[28:29], v[28:29], v[36:37]
	v_lshlrev_b32_e32 v36, 16, v42
	v_and_b32_e32 v37, 0xffff0000, v42
	v_lshlrev_b32_e32 v38, 16, v43
	v_and_b32_e32 v39, 0xffff0000, v43
	v_pk_mul_f32 v[22:23], v[22:23], v[34:35]
	v_pk_mul_f32 v[16:17], v[20:21], v[16:17]
	v_pk_mul_f32 v[34:35], v[22:23], v[38:39]
	v_pk_mul_f32 v[22:23], v[16:17], v[36:37]
	v_cvt_pk_bf16_f32 v16, v24, v25
	v_add_u32_e32 v24, 0xb0, v152
	v_ashrrev_i32_e32 v25, 31, v24
	v_lshlrev_b64 v[24:25], 11, v[24:25]
	v_lshl_add_u64 v[24:25], s[6:7], 0, v[24:25]
	v_cvt_pk_bf16_f32 v17, v26, v27
	v_cvt_pk_bf16_f32 v18, v18, v19
	v_cvt_pk_bf16_f32 v19, v32, v33
	v_cvt_pk_bf16_f32 v20, v28, v29
	v_cvt_pk_bf16_f32 v21, v30, v31
	v_cvt_pk_bf16_f32 v22, v22, v23
	v_cvt_pk_bf16_f32 v23, v34, v35
	v_lshl_add_u64 v[24:25], v[24:25], 0, v[154:155]
	v_mov_b64_e32 v[24:25], v[220:221]
	v_mov_b64_e32 v[26:27], v[222:223]
	v_fmamk_f32 v8, v8, 0xbfb8aa3b, v150
	v_fmac_f32_e32 v151, 0xbfb8aa3b, v9
	v_exp_f32_e32 v8, v8
	v_exp_f32_e32 v9, v151
	v_fmamk_f32 v10, v10, 0xbfb8aa3b, v148
	v_fmac_f32_e32 v149, 0xbfb8aa3b, v11
	v_exp_f32_e32 v10, v10
	v_exp_f32_e32 v11, v149
	v_pk_add_f32 v[8:9], v[8:9], 1.0 op_sel_hi:[1,0]
	v_lshl_add_u64 v[28:29], v[114:115], 0, s[26:27]
	v_rcp_f32_e32 v8, v8
	v_pk_add_f32 v[10:11], v[10:11], 1.0 op_sel_hi:[1,0]
	v_rcp_f32_e32 v9, v9
	v_rcp_f32_e32 v10, v10
	v_rcp_f32_e32 v11, v11
	v_lshl_add_u64 v[30:31], s[40:41], 0, v[28:29]
	global_store_dwordx4 v[30:31], v[16:19], off
	v_pk_mul_f32 v[8:9], v[120:121], v[8:9]
	v_pk_mul_f32 v[10:11], v[122:123], v[10:11]
	v_lshl_add_u64 v[16:17], s[42:43], 0, v[28:29]
	global_store_dwordx4 v[16:17], v[20:23], off
	v_mul_f32_e32 v16, 0x4038aa3b, v8
	v_mul_f32_e32 v17, 0x4038aa3b, v9
	v_fmamk_f32 v12, v12, 0xbfb8aa3b, v158
	v_fmac_f32_e32 v159, 0xbfb8aa3b, v13
	v_fmamk_f32 v13, v14, 0xbfb8aa3b, v156
	v_mul_f32_e32 v18, 0x4038aa3b, v10
	v_mul_f32_e32 v19, 0x4038aa3b, v11
	v_exp_f32_e32 v17, v17
	v_exp_f32_e32 v16, v16
	v_fmamk_f32 v0, v0, 0xbfb8aa3b, v142
	v_fmac_f32_e32 v143, 0xbfb8aa3b, v1
	v_fmamk_f32 v2, v2, 0xbfb8aa3b, v140
	v_fmac_f32_e32 v141, 0xbfb8aa3b, v3
	v_exp_f32_e32 v12, v12
	v_exp_f32_e32 v14, v13
	v_fmac_f32_e32 v157, 0xbfb8aa3b, v15
	v_exp_f32_e32 v13, v159
	v_exp_f32_e32 v19, v19
	v_exp_f32_e32 v18, v18
	v_exp_f32_e32 v0, v0
	v_exp_f32_e32 v1, v143
	v_exp_f32_e32 v2, v2
	v_exp_f32_e32 v3, v141
	v_exp_f32_e32 v15, v157
	v_sub_f32_e32 v17, 1.0, v17
	v_sub_f32_e32 v16, 1.0, v16
	v_pk_add_f32 v[12:13], v[12:13], 1.0 op_sel_hi:[1,0]
	v_sub_f32_e32 v19, 1.0, v19
	v_sub_f32_e32 v18, 1.0, v18
	v_max_f32_e32 v16, 0, v16
	v_max_f32_e32 v17, 0, v17
	v_pk_add_f32 v[2:3], v[2:3], 1.0 op_sel_hi:[1,0]
	v_pk_add_f32 v[0:1], v[0:1], 1.0 op_sel_hi:[1,0]
	v_pk_add_f32 v[14:15], v[14:15], 1.0 op_sel_hi:[1,0]
	v_rcp_f32_e32 v12, v12
	v_rcp_f32_e32 v13, v13
	v_sqrt_f32_e32 v16, v16
	v_sqrt_f32_e32 v17, v17
	v_max_f32_e32 v18, 0, v18
	v_max_f32_e32 v19, 0, v19
	v_rcp_f32_e32 v0, v0
	v_rcp_f32_e32 v1, v1
	v_rcp_f32_e32 v2, v2
	v_rcp_f32_e32 v3, v3
	v_rcp_f32_e32 v14, v14
	v_rcp_f32_e32 v15, v15
	v_sqrt_f32_e32 v18, v18
	v_sqrt_f32_e32 v19, v19
	v_pk_mul_f32 v[12:13], v[12:13], v[16:17]
	v_pk_mul_f32 v[16:17], v[112:113], v[2:3]
	v_pk_mul_f32 v[2:3], v[116:117], v[0:1]
	v_pk_mul_f32 v[14:15], v[14:15], v[18:19]
	v_mul_f32_e32 v0, 0x4038aa3b, v2
	v_mul_f32_e32 v1, 0x4038aa3b, v3
	v_mul_f32_e32 v18, 0x4038aa3b, v16
	v_mul_f32_e32 v19, 0x4038aa3b, v17
	v_fmamk_f32 v4, v4, 0xbfb8aa3b, v146
	v_fmac_f32_e32 v147, 0xbfb8aa3b, v5
	v_fmamk_f32 v5, v6, 0xbfb8aa3b, v144
	v_fmac_f32_e32 v145, 0xbfb8aa3b, v7
	v_exp_f32_e32 v19, v19
	v_exp_f32_e32 v18, v18
	v_exp_f32_e32 v1, v1
	v_exp_f32_e32 v0, v0
	v_exp_f32_e32 v4, v4
	v_exp_f32_e32 v6, v5
	v_exp_f32_e32 v7, v145
	v_exp_f32_e32 v5, v147
	v_sub_f32_e32 v19, 1.0, v19
	v_sub_f32_e32 v18, 1.0, v18
	v_sub_f32_e32 v1, 1.0, v1
	v_sub_f32_e32 v0, 1.0, v0
	v_pk_add_f32 v[6:7], v[6:7], 1.0 op_sel_hi:[1,0]
	v_pk_add_f32 v[4:5], v[4:5], 1.0 op_sel_hi:[1,0]
	v_max_f32_e32 v0, 0, v0
	v_max_f32_e32 v1, 0, v1
	v_max_f32_e32 v18, 0, v18
	v_max_f32_e32 v19, 0, v19
	v_rcp_f32_e32 v4, v4
	v_rcp_f32_e32 v5, v5
	v_rcp_f32_e32 v6, v6
	v_rcp_f32_e32 v7, v7
	v_sqrt_f32_e32 v0, v0
	v_sqrt_f32_e32 v1, v1
	v_sqrt_f32_e32 v18, v18
	v_sqrt_f32_e32 v19, v19
	s_waitcnt vmcnt(2)
	v_lshlrev_b32_e32 v20, 16, v24
	v_and_b32_e32 v21, 0xffff0000, v24
	v_lshlrev_b32_e32 v22, 16, v25
	v_and_b32_e32 v23, 0xffff0000, v25
	v_pk_mul_f32 v[14:15], v[14:15], v[22:23]
	v_pk_mul_f32 v[12:13], v[12:13], v[20:21]
	v_lshlrev_b32_e32 v20, 16, v26
	v_and_b32_e32 v21, 0xffff0000, v26
	v_lshlrev_b32_e32 v22, 16, v27
	v_and_b32_e32 v23, 0xffff0000, v27
	v_pk_mul_f32 v[6:7], v[6:7], v[18:19]
	v_pk_mul_f32 v[0:1], v[4:5], v[0:1]
	v_pk_mul_f32 v[18:19], v[6:7], v[22:23]
	v_pk_mul_f32 v[6:7], v[0:1], v[20:21]
	v_cvt_pk_bf16_f32 v0, v8, v9
	v_lshl_add_u64 v[8:9], v[114:115], 0, s[28:29]
	v_cvt_pk_bf16_f32 v1, v10, v11
	v_cvt_pk_bf16_f32 v2, v2, v3
	v_cvt_pk_bf16_f32 v3, v16, v17
	v_cvt_pk_bf16_f32 v4, v12, v13
	v_cvt_pk_bf16_f32 v5, v14, v15
	v_cvt_pk_bf16_f32 v6, v6, v7
	v_cvt_pk_bf16_f32 v7, v18, v19
	v_lshl_add_u64 v[10:11], s[40:41], 0, v[8:9]
	global_store_dwordx4 v[10:11], v[0:3], off
	s_nop 1
	v_lshl_add_u64 v[0:1], s[42:43], 0, v[8:9]
	global_store_dwordx4 v[0:1], v[4:7], off
	s_cbranch_vccnz .LBB0_2340
	s_andn2_b64 vcc, exec, s[8:9]
	s_cbranch_vccnz .LBB0_2339
	s_barrier
	s_branch .LBB0_2339

	.amdhsa_kernel _Z6mk_fwd4Args
		.amdhsa_group_segment_fixed_size 0
		.amdhsa_private_segment_fixed_size 0
		.amdhsa_kernarg_size 520
		.amdhsa_user_sgpr_count 2
		.amdhsa_user_sgpr_dispatch_ptr 0
		.amdhsa_user_sgpr_queue_ptr 0
		.amdhsa_user_sgpr_kernarg_segment_ptr 1
		.amdhsa_user_sgpr_dispatch_id 0
		.amdhsa_user_sgpr_kernarg_preload_length 0
		.amdhsa_user_sgpr_kernarg_preload_offset 0
		.amdhsa_user_sgpr_private_segment_size 0
		.amdhsa_uses_dynamic_stack 0
		.amdhsa_enable_private_segment 0
		.amdhsa_system_sgpr_workgroup_id_x 1
		.amdhsa_system_sgpr_workgroup_id_y 0
		.amdhsa_system_sgpr_workgroup_id_z 0
		.amdhsa_system_sgpr_workgroup_info 0
		.amdhsa_system_vgpr_workitem_id 0
		.amdhsa_next_free_vgpr 255
		.amdhsa_next_free_sgpr 102
		.amdhsa_accum_offset 256
		.amdhsa_reserve_vcc 1
		.amdhsa_float_round_mode_32 0
		.amdhsa_float_round_mode_16_64 0
		.amdhsa_float_denorm_mode_32 3
		.amdhsa_float_denorm_mode_16_64 3
		.amdhsa_dx10_clamp 1
		.amdhsa_ieee_mode 1
		.amdhsa_fp16_overflow 0
		.amdhsa_tg_split 0
		.amdhsa_exception_fp_ieee_invalid_op 0
		.amdhsa_exception_fp_denorm_src 0
		.amdhsa_exception_fp_ieee_div_zero 0
		.amdhsa_exception_fp_ieee_overflow 0
		.amdhsa_exception_fp_ieee_underflow 0
		.amdhsa_exception_fp_ieee_inexact 0
		.amdhsa_exception_int_div_zero 0
	.end_amdhsa_kernel

amdhsa.kernels:
  - .agpr_count:     0
    .args:
      - .offset:         0
        .size:           264
        .value_kind:     by_value
      - .offset:         264
        .size:           4
        .value_kind:     hidden_block_count_x
      - .offset:         268
        .size:           4
        .value_kind:     hidden_block_count_y
      - .offset:         272
        .size:           4
        .value_kind:     hidden_block_count_z
      - .offset:         276
        .size:           2
        .value_kind:     hidden_group_size_x
      - .offset:         278
        .size:           2
        .value_kind:     hidden_group_size_y
      - .offset:         280
        .size:           2
        .value_kind:     hidden_group_size_z
      - .offset:         282
        .size:           2
        .value_kind:     hidden_remainder_x
      - .offset:         284
        .size:           2
        .value_kind:     hidden_remainder_y
      - .offset:         286
        .size:           2
        .value_kind:     hidden_remainder_z
      - .offset:         304
        .size:           8
        .value_kind:     hidden_global_offset_x
      - .offset:         312
        .size:           8
        .value_kind:     hidden_global_offset_y
      - .offset:         320
        .size:           8
        .value_kind:     hidden_global_offset_z
      - .offset:         328
        .size:           2
        .value_kind:     hidden_grid_dims
      - .offset:         384
        .size:           4
        .value_kind:     hidden_dynamic_lds_size
    .group_segment_fixed_size: 0
    .kernarg_segment_align: 8
    .kernarg_segment_size: 520
    .language:       OpenCL C
    .language_version:
      - 2
      - 0
    .max_flat_workgroup_size: 512
    .name:           _Z6mk_fwd4Args
    .private_segment_fixed_size: 0
    .sgpr_count:     108
    .sgpr_spill_count: 32
    .symbol:         _Z6mk_fwd4Args.kd
    .uniform_work_group_size: 1
    .uses_dynamic_stack: false
    .vgpr_count:     255
    .vgpr_spill_count: 0
    .wavefront_size: 64
